# nt hint on weight-conversion f32 loads and fp8 stores
# speedup vs baseline: 1.0047x; 1.0047x over previous
; #define GAS __attribute__((address_space(1)))
; #define LAS __attribute__((address_space(3)))
; __device__ __forceinline__ void titem_load(const TItem& T, int lane, f32x4 (&v)[8]) {
;     const int nblk = T.N / 32, kb = T.item / nblk, nb = T.item % nblk, k0 = 64 * kb, n0 = 32 * nb;
; #pragma unroll
;     for (int i = 0; i < 8; ++i) v[i] = *(const GAS f32x4*)(T.W + (size_t)(k0 + 8 * i + (lane >> 3)) * T.N + n0 + 4 * (lane & 7));
; }
; __device__ __forceinline__ void titem_store(const TItem& T, int lane, const f32x4 (&v)[8], LAS float* scr) {
;     const int nblk = T.N / 32, kb = T.item / nblk, nb = T.item % nblk, k0 = 64 * kb, n0 = 32 * nb;
; #pragma unroll
;     for (int i = 0; i < 8; ++i) { LAS float* s = scr + (8 * i + (lane >> 3)) * 33 + 4 * (lane & 7); s[0] = v[i][0]; s[1] = v[i][1]; s[2] = v[i][2]; s[3] = v[i][3]; }
;     LDS_WAIT(); asm volatile("" ::: "memory");
;     const int c = lane & 7;
; #pragma unroll
;     for (int j = 0; j < 4; ++j) { const int n = (lane >> 3) + 8 * j; const LAS float* s = scr + (8 * c) * 33 + n;
;         if (T.f8) { u32x2 o; o.x = pg8::pack4_fp8(s[0 * 33] * pg8::SC_W, s[1 * 33] * pg8::SC_W, s[2 * 33] * pg8::SC_W, s[3 * 33] * pg8::SC_W); o.y = pg8::pack4_fp8(s[4 * 33] * pg8::SC_W, s[5 * 33] * pg8::SC_W, s[6 * 33] * pg8::SC_W, s[7 * 33] * pg8::SC_W);
;             *(GAS u32x2*)((unsigned char*)T.WT + (size_t)row_map(T.mode, n0, n) * 1024 + k0 + 8 * c) = o; }
;         else { u32x4 o; o.x = pk2(s[0 * 33], s[1 * 33]); o.y = pk2(s[2 * 33], s[3 * 33]); o.z = pk2(s[4 * 33], s[5 * 33]); o.w = pk2(s[6 * 33], s[7 * 33]);
;             *(GAS u32x4*)(T.WT + (size_t)row_map(T.mode, n0, n) * 1024 + k0 + 8 * c) = o; } }
;     LDS_WAIT(); asm volatile("" ::: "memory");
; }
; __device__ __forceinline__ void p0_prologue(const Frame& F0) {
;     ...
;         for (int it = gw; it < NITEMS; it += NGW) {
;             if (it >= NSMALL) break;
;             int r = it; const int j = r >= NSMALL / 2 ? 1 : 0; r -= j * (NSMALL / 2);
;             if (r < I_AIN) { p0_transpose_item(inp(F, I_AWIN) + (size_t)j * 1024 * 1536, 1536, (bf16_t*)(ws + WS_WAIN + (size_t)j * 1536 * 1024), RM_AIN, scr, r, F.lane, true); continue; } r -= I_AIN;
;             if (r < I_SQ) { p0_transpose_item(inp(F, I_AWOUT) + (size_t)j * 1024 * 1024, 1024, (bf16_t*)(ws + WS_WAOUT + (size_t)j * 1024 * 1024), RM_P8, scr, r, F.lane, true); continue; } r -= I_SQ;
.LBB0_50:
	s_cmpk_gt_i32 s43, 0xcff
	s_cselect_b64 s[2:3], -1, 0
	s_and_b64 s[4:5], s[2:3], exec
	s_cselect_b32 s44, 0xfffff300, 0
	s_add_i32 s44, s44, s43
	s_cmpk_gt_i32 s44, 0x2ff
	s_mov_b64 s[4:5], -1
	s_cbranch_scc0 .LBB0_60
	s_cmpk_gt_u32 s44, 0x4ff
	s_cbranch_scc0 .LBB0_57
	s_cmpk_gt_u32 s44, 0xaff
	s_cbranch_scc0 .LBB0_54
	v_mov_b32_e32 v7, s21
	s_waitcnt vmcnt(0)
	ds_read_b64 v[34:35], v7
	s_and_b64 s[4:5], s[2:3], exec
	s_cselect_b32 s0, 0x100000, 0
	s_lshl_b32 s4, s0, 2
	s_mov_b32 s7, s1
	s_waitcnt lgkmcnt(0)
	v_readfirstlane_b32 s5, v34
	v_readfirstlane_b32 s6, v35
	s_add_u32 s46, s5, s4
	s_addc_u32 s47, s6, 0
	s_lshl_b32 s0, s0, 1
	s_add_u32 s4, s8, s0
	s_addc_u32 s5, s9, 0
	s_lshl_b32 s0, s44, 1
	s_andn2_b32 s0, s0, 63
	s_add_i32 s6, s0, 0xffffea00
	v_or_b32_e32 v62, s6, v70
	v_or_b32_e32 v36, 8, v62
	v_or_b32_e32 v42, 16, v62
	v_or_b32_e32 v44, 24, v62
	v_or_b32_e32 v50, 32, v62
	v_or_b32_e32 v52, 40, v62
	v_ashrrev_i32_e32 v63, 31, v62
	v_ashrrev_i32_e32 v37, 31, v36
	v_ashrrev_i32_e32 v43, 31, v42
	v_ashrrev_i32_e32 v45, 31, v44
	v_ashrrev_i32_e32 v51, 31, v50
	v_ashrrev_i32_e32 v53, 31, v52
	s_and_b32 s45, s19, 0x3e0
	v_lshlrev_b64 v[34:35], 12, v[62:63]
	v_lshlrev_b64 v[36:37], 12, v[36:37]
	v_lshlrev_b64 v[42:43], 12, v[42:43]
	v_lshlrev_b64 v[44:45], 12, v[44:45]
	v_lshlrev_b64 v[50:51], 12, v[50:51]
	v_lshlrev_b64 v[52:53], 12, v[52:53]
	v_lshl_add_u64 v[34:35], s[46:47], 0, v[34:35]
	s_lshl_b32 s0, s45, 2
	v_lshl_add_u64 v[36:37], s[46:47], 0, v[36:37]
	v_lshl_add_u64 v[42:43], s[46:47], 0, v[42:43]
	v_lshl_add_u64 v[44:45], s[46:47], 0, v[44:45]
	v_lshl_add_u64 v[50:51], s[46:47], 0, v[50:51]
	v_lshl_add_u64 v[52:53], s[46:47], 0, v[52:53]
	v_lshl_add_u64 v[34:35], v[34:35], 0, s[0:1]
	v_lshl_add_u64 v[36:37], v[36:37], 0, s[0:1]
	v_lshl_add_u64 v[42:43], v[42:43], 0, s[0:1]
	v_lshl_add_u64 v[44:45], v[44:45], 0, s[0:1]
	v_lshl_add_u64 v[50:51], v[50:51], 0, s[0:1]
	v_lshl_add_u64 v[52:53], v[52:53], 0, s[0:1]
	v_lshl_add_u64 v[34:35], v[34:35], 0, v[2:3]
	v_lshl_add_u64 v[38:39], v[36:37], 0, v[2:3]
	v_lshl_add_u64 v[42:43], v[42:43], 0, v[2:3]
	v_lshl_add_u64 v[46:47], v[44:45], 0, v[2:3]
	v_lshl_add_u64 v[50:51], v[50:51], 0, v[2:3]
	v_lshl_add_u64 v[54:55], v[52:53], 0, v[2:3]
	global_load_dwordx4 v[34:37], v[34:35], off nt
	s_nop 0
	global_load_dwordx4 v[38:41], v[38:39], off nt
	s_nop 0
	global_load_dwordx4 v[42:45], v[42:43], off nt
	s_nop 0
	global_load_dwordx4 v[46:49], v[46:47], off nt
	s_nop 0
	global_load_dwordx4 v[50:53], v[50:51], off nt
	s_nop 0
	global_load_dwordx4 v[54:57], v[54:55], off nt
	v_or_b32_e32 v58, 48, v62
	v_ashrrev_i32_e32 v59, 31, v58
	v_lshlrev_b64 v[58:59], 12, v[58:59]
	v_or_b32_e32 v62, 56, v62
	v_lshl_add_u64 v[58:59], s[46:47], 0, v[58:59]
	v_ashrrev_i32_e32 v63, 31, v62
	v_lshl_add_u64 v[58:59], v[58:59], 0, s[0:1]
	v_lshlrev_b64 v[62:63], 12, v[62:63]
	v_lshl_add_u64 v[58:59], v[58:59], 0, v[2:3]
	v_lshl_add_u64 v[62:63], s[46:47], 0, v[62:63]
	global_load_dwordx4 v[58:61], v[58:59], off nt
	v_lshl_add_u64 v[62:63], v[62:63], 0, s[0:1]
	v_lshl_add_u64 v[62:63], v[62:63], 0, v[2:3]
	global_load_dwordx4 v[62:65], v[62:63], off nt
	v_or_b32_e32 v68, s45, v1
	v_or_b32_e32 v7, v68, v14
	v_mov_b32_e32 v67, v3
	v_lshlrev_b32_e32 v66, 11, v7
	s_lshl_b64 s[6:7], s[6:7], 1
	v_mov_b32_e32 v7, v3
	s_waitcnt vmcnt(7)
	ds_write2_b32 v18, v34, v35 offset1:1
	ds_write2_b32 v18, v36, v37 offset0:2 offset1:3
	s_waitcnt vmcnt(6)
	ds_write2_b32 v19, v38, v39 offset1:1
	ds_write2_b32 v20, v40, v41 offset1:1
	s_waitcnt vmcnt(5)
	ds_write2_b32 v21, v42, v43 offset1:1
	ds_write2_b32 v22, v44, v45 offset1:1
	s_waitcnt vmcnt(4)
	ds_write2_b32 v23, v46, v47 offset1:1
	ds_write2_b32 v24, v48, v49 offset1:1
	s_waitcnt vmcnt(3)
	ds_write2_b32 v25, v50, v51 offset1:1
	ds_write2_b32 v26, v52, v53 offset1:1
	s_waitcnt vmcnt(2)
	ds_write2_b32 v27, v54, v55 offset1:1
	ds_write2_b32 v28, v56, v57 offset1:1
	s_waitcnt vmcnt(1)
	ds_write2_b32 v29, v58, v59 offset1:1
	ds_write2_b32 v30, v60, v61 offset1:1
	s_waitcnt vmcnt(0)
	ds_write2_b32 v31, v62, v63 offset1:1
	ds_write2_b32 v32, v64, v65 offset1:1
	s_waitcnt lgkmcnt(0)
	ds_read2_b32 v[38:39], v13 offset0:33 offset1:41
	ds_read2_b32 v[40:41], v13 offset1:8
	ds_read2_b32 v[42:43], v13 offset0:66 offset1:74
	ds_read2_b32 v[44:45], v13 offset0:99 offset1:107
	ds_read2_b32 v[46:47], v13 offset0:132 offset1:140
	ds_read2_b32 v[48:49], v13 offset0:165 offset1:173
	ds_read2_b32 v[50:51], v13 offset0:198 offset1:206
	ds_read2_b32 v[52:53], v13 offset0:231 offset1:239
	v_lshl_add_u64 v[54:55], s[4:5], 0, v[66:67]
	v_lshl_add_u64 v[54:55], v[54:55], 0, s[6:7]
	v_lshl_add_u64 v[54:55], v[54:55], 0, v[6:7]
	s_waitcnt lgkmcnt(6)
	v_cvt_pk_bf16_f32 v34, v40, v38
	s_waitcnt lgkmcnt(4)
	v_cvt_pk_bf16_f32 v35, v42, v44
	s_waitcnt lgkmcnt(2)
	v_cvt_pk_bf16_f32 v36, v46, v48
	s_waitcnt lgkmcnt(0)
	v_cvt_pk_bf16_f32 v37, v50, v52
	global_store_dwordx4 v[54:55], v[34:37], off
	v_add_co_u32_e32 v38, vcc, s22, v54
	s_nop 0
	v_cvt_pk_bf16_f32 v34, v41, v39
	v_cvt_pk_bf16_f32 v35, v43, v45
	v_cvt_pk_bf16_f32 v36, v47, v49
	v_cvt_pk_bf16_f32 v37, v51, v53
	ds_read2_b32 v[40:41], v13 offset0:16 offset1:24
	ds_read2_b32 v[42:43], v13 offset0:49 offset1:57
	ds_read2_b32 v[44:45], v13 offset0:82 offset1:90
	ds_read2_b32 v[46:47], v13 offset0:115 offset1:123
	ds_read2_b32 v[48:49], v13 offset0:148 offset1:156
	ds_read2_b32 v[50:51], v13 offset0:181 offset1:189
	ds_read2_b32 v[52:53], v13 offset0:214 offset1:222
	ds_read2_b32 v[56:57], v13 offset0:247 offset1:255
	v_addc_co_u32_e32 v39, vcc, 0, v55, vcc
	global_store_dwordx4 v[38:39], v[34:37], off
	v_add_co_u32_e32 v38, vcc, s23, v54
	s_waitcnt lgkmcnt(6)
	v_cvt_pk_bf16_f32 v34, v40, v42
	s_waitcnt lgkmcnt(4)
	v_cvt_pk_bf16_f32 v35, v44, v46
	s_waitcnt lgkmcnt(2)
	v_cvt_pk_bf16_f32 v36, v48, v50
	s_waitcnt lgkmcnt(0)
	v_cvt_pk_bf16_f32 v37, v52, v56
	v_addc_co_u32_e32 v39, vcc, 0, v55, vcc
	global_store_dwordx4 v[38:39], v[34:37], off
	v_lshl_or_b32 v38, v68, 11, v15
	v_mov_b32_e32 v39, v3
	v_lshl_add_u64 v[38:39], s[4:5], 0, v[38:39]
	v_lshl_add_u64 v[38:39], v[38:39], 0, s[6:7]
	v_lshl_add_u64 v[38:39], v[38:39], 0, v[6:7]
	v_cvt_pk_bf16_f32 v34, v41, v43
	v_cvt_pk_bf16_f32 v35, v45, v47
	v_cvt_pk_bf16_f32 v36, v49, v51
	v_cvt_pk_bf16_f32 v37, v53, v57
	global_store_dwordx4 v[38:39], v[34:37], off
	s_waitcnt lgkmcnt(0)
	s_mov_b64 s[4:5], 0
; #define GAS __attribute__((address_space(1)))
; #define LAS __attribute__((address_space(3)))
; __device__ __forceinline__ int row_map(int mode, int l0, int x) {
;     switch (mode) {
;     case RM_NAT: return l0 + x;
;     case RM_AIN: return (l0 & ~255) + ((l0 >> 5) & 1) * 128 + ((l0 >> 6) & 3) * 32 + x;
;     case RM_P8:  return l0 + inv32(x);
;     case RM_CIN: if (l0 < 1024) return l0 + inv32(x);
;                  else { const int j = (l0 - 1024) & 1023, isv = (l0 >= 2048); return 1024 + 256 * (j >> 7) + 128 * isv + 32 * ((j >> 5) & 3) + inv32(x); }
;     case RM_UPG: return 256 * (l0 >> 7) + 32 * ((l0 >> 5) & 3) + inv32(x);
;     default:     return 256 * (l0 >> 7) + 128 + 32 * ((l0 >> 5) & 3) + inv32(x);
;     }
; }
; __device__ __forceinline__ void titem_load(const TItem& T, int lane, f32x4 (&v)[8]) {
;     const int nblk = T.N / 32, kb = T.item / nblk, nb = T.item % nblk, k0 = 64 * kb, n0 = 32 * nb;
; #pragma unroll
;     for (int i = 0; i < 8; ++i) v[i] = *(const GAS f32x4*)(T.W + (size_t)(k0 + 8 * i + (lane >> 3)) * T.N + n0 + 4 * (lane & 7));
; }
; __device__ __forceinline__ void titem_store(const TItem& T, int lane, const f32x4 (&v)[8], LAS float* scr) {
;     const int nblk = T.N / 32, kb = T.item / nblk, nb = T.item % nblk, k0 = 64 * kb, n0 = 32 * nb;
; #pragma unroll
;     for (int i = 0; i < 8; ++i) { LAS float* s = scr + (8 * i + (lane >> 3)) * 33 + 4 * (lane & 7); s[0] = v[i][0]; s[1] = v[i][1]; s[2] = v[i][2]; s[3] = v[i][3]; }
;     LDS_WAIT(); asm volatile("" ::: "memory");
;     const int c = lane & 7;
; #pragma unroll
;     for (int j = 0; j < 4; ++j) { const int n = (lane >> 3) + 8 * j; const LAS float* s = scr + (8 * c) * 33 + n;
;         if (T.f8) { u32x2 o; o.x = pg8::pack4_fp8(s[0 * 33] * pg8::SC_W, s[1 * 33] * pg8::SC_W, s[2 * 33] * pg8::SC_W, s[3 * 33] * pg8::SC_W); o.y = pg8::pack4_fp8(s[4 * 33] * pg8::SC_W, s[5 * 33] * pg8::SC_W, s[6 * 33] * pg8::SC_W, s[7 * 33] * pg8::SC_W);
;             *(GAS u32x2*)((unsigned char*)T.WT + (size_t)row_map(T.mode, n0, n) * 1024 + k0 + 8 * c) = o; }
;         else { u32x4 o; o.x = pk2(s[0 * 33], s[1 * 33]); o.y = pk2(s[2 * 33], s[3 * 33]); o.z = pk2(s[4 * 33], s[5 * 33]); o.w = pk2(s[6 * 33], s[7 * 33]);
;             *(GAS u32x4*)(T.WT + (size_t)row_map(T.mode, n0, n) * 1024 + k0 + 8 * c) = o; } }
;     LDS_WAIT(); asm volatile("" ::: "memory");
; }
.LBB0_54:
	s_andn2_b64 vcc, exec, s[4:5]
	s_cbranch_vccnz .LBB0_56
	v_mov_b32_e32 v7, s25
	s_waitcnt vmcnt(0)
	ds_read_b64 v[34:35], v7
	s_and_b64 s[4:5], s[2:3], exec
	s_cselect_b32 s0, 0x300000, 0
	s_lshl_b32 s4, s0, 2
	v_mov_b32_e32 v67, v3
	s_waitcnt lgkmcnt(0)
	v_readfirstlane_b32 s5, v34
	v_readfirstlane_b32 s7, v35
	s_add_u32 s6, s5, s4
	s_addc_u32 s7, s7, 0
	s_lshl_b32 s0, s0, 1
	s_add_u32 s4, s11, s0
	s_addc_u32 s5, s12, 0
	s_add_i32 s0, s44, 0xfb00
	s_and_b32 s45, s0, 0xffff
	s_mul_i32 s45, s45, 0xaaab
	s_lshr_b32 s46, s45, 16
	s_lshr_b32 s45, s45, 22
	s_and_b32 s46, s46, 0xffc0
	s_mulk_i32 s45, 0x60
	v_or_b32_e32 v7, s46, v70
	s_sub_i32 s0, s0, s45
	v_mul_u32_u24_e32 v7, 0xc00, v7
	s_and_b32 s45, s0, 0xffff
	v_lshlrev_b32_e32 v34, 2, v7
	v_mov_b32_e32 v35, v3
	v_lshl_add_u64 v[34:35], s[6:7], 0, v[34:35]
	s_lshl_b32 s0, s45, 7
	v_lshl_add_u64 v[34:35], v[34:35], 0, s[0:1]
	v_lshl_add_u64 v[62:63], v[34:35], 0, v[2:3]
	v_add_co_u32_e32 v38, vcc, s26, v62
	s_lshl_b32 s0, s45, 5
	s_nop 0
	v_addc_co_u32_e32 v39, vcc, 0, v63, vcc
	v_add_co_u32_e32 v42, vcc, s27, v62
	global_load_dwordx4 v[34:37], v[62:63], off nt
	s_nop 0
	global_load_dwordx4 v[38:41], v[38:39], off nt
	v_addc_co_u32_e32 v43, vcc, 0, v63, vcc
	v_add_co_u32_e32 v46, vcc, s28, v62
	s_lshl_b32 s6, s45, 6
	s_nop 0
	v_addc_co_u32_e32 v47, vcc, 0, v63, vcc
	v_add_co_u32_e32 v50, vcc, s29, v62
	global_load_dwordx4 v[42:45], v[42:43], off nt
	s_nop 0
	global_load_dwordx4 v[46:49], v[46:47], off nt
	v_addc_co_u32_e32 v51, vcc, 0, v63, vcc
	v_add_co_u32_e32 v54, vcc, s30, v62
	s_and_b32 s7, s0, 0x60
	s_nop 0
	v_addc_co_u32_e32 v55, vcc, 0, v63, vcc
	global_load_dwordx4 v[50:53], v[50:51], off nt
	s_nop 0
	global_load_dwordx4 v[54:57], v[54:55], off nt
	v_add_co_u32_e32 v58, vcc, s31, v62
	s_and_b32 s6, s6, 0x700
	s_nop 0
	v_addc_co_u32_e32 v59, vcc, 0, v63, vcc
	global_load_dwordx4 v[58:61], v[58:59], off nt
	v_add_co_u32_e32 v62, vcc, s33, v62
	s_cmp_gt_u32 s45, 63
	s_nop 0
	v_addc_co_u32_e32 v63, vcc, 0, v63, vcc
	global_load_dwordx4 v[62:65], v[62:63], off nt
	s_cselect_b32 s47, 0x80, 0
	s_or_b32 s6, s6, s47
	s_or_b32 s6, s6, s7
	s_addk_i32 s6, 0x400
	s_cmp_lt_u32 s45, 32
	s_cselect_b32 s0, s0, s6
	v_or_b32_e32 v71, s0, v1
	v_or_b32_e32 v66, v71, v14
	v_lshlrev_b64 v[68:69], 11, v[66:67]
	s_lshl_b32 s0, s46, 1
	v_mov_b32_e32 v7, v3
	s_waitcnt vmcnt(7)
	ds_write2_b32 v18, v34, v35 offset1:1
	ds_write2_b32 v18, v36, v37 offset0:2 offset1:3
	s_waitcnt vmcnt(6)
	ds_write2_b32 v19, v38, v39 offset1:1
	ds_write2_b32 v20, v40, v41 offset1:1
	s_waitcnt vmcnt(5)
	ds_write2_b32 v21, v42, v43 offset1:1
	ds_write2_b32 v22, v44, v45 offset1:1
	s_waitcnt vmcnt(4)
	ds_write2_b32 v23, v46, v47 offset1:1
	ds_write2_b32 v24, v48, v49 offset1:1
	s_waitcnt vmcnt(3)
	ds_write2_b32 v25, v50, v51 offset1:1
	ds_write2_b32 v26, v52, v53 offset1:1
	s_waitcnt vmcnt(2)
	ds_write2_b32 v27, v54, v55 offset1:1
	ds_write2_b32 v28, v56, v57 offset1:1
	s_waitcnt vmcnt(1)
	ds_write2_b32 v29, v58, v59 offset1:1
	ds_write2_b32 v30, v60, v61 offset1:1
	s_waitcnt vmcnt(0)
	ds_write2_b32 v31, v62, v63 offset1:1
	ds_write2_b32 v32, v64, v65 offset1:1
	s_waitcnt lgkmcnt(0)
	ds_read2_b32 v[38:39], v13 offset0:33 offset1:41
	ds_read2_b32 v[40:41], v13 offset1:8
	ds_read2_b32 v[42:43], v13 offset0:66 offset1:74
	ds_read2_b32 v[44:45], v13 offset0:99 offset1:107
	ds_read2_b32 v[46:47], v13 offset0:132 offset1:140
	ds_read2_b32 v[48:49], v13 offset0:165 offset1:173
	ds_read2_b32 v[50:51], v13 offset0:198 offset1:206
	ds_read2_b32 v[52:53], v13 offset0:231 offset1:239
	v_lshl_add_u64 v[54:55], s[4:5], 0, v[68:69]
	v_lshl_add_u64 v[54:55], v[54:55], 0, s[0:1]
	s_waitcnt lgkmcnt(6)
	v_cvt_pk_bf16_f32 v34, v40, v38
	v_lshl_add_u64 v[54:55], v[54:55], 0, v[6:7]
	s_waitcnt lgkmcnt(4)
	v_cvt_pk_bf16_f32 v35, v42, v44
	s_waitcnt lgkmcnt(2)
	v_cvt_pk_bf16_f32 v36, v46, v48
	s_waitcnt lgkmcnt(0)
	v_cvt_pk_bf16_f32 v37, v50, v52
	global_store_dwordx4 v[54:55], v[34:37], off
	v_or_b32_e32 v38, 4, v66
	s_nop 0
	v_cvt_pk_bf16_f32 v34, v41, v39
	v_mov_b32_e32 v39, v3
	v_lshlrev_b64 v[38:39], 11, v[38:39]
	v_lshl_add_u64 v[38:39], s[4:5], 0, v[38:39]
	v_lshl_add_u64 v[38:39], v[38:39], 0, s[0:1]
	v_lshl_add_u64 v[38:39], v[38:39], 0, v[6:7]
	v_cvt_pk_bf16_f32 v35, v43, v45
	v_cvt_pk_bf16_f32 v36, v47, v49
	v_cvt_pk_bf16_f32 v37, v51, v53
	ds_read2_b32 v[40:41], v13 offset0:16 offset1:24
	ds_read2_b32 v[42:43], v13 offset0:49 offset1:57
	ds_read2_b32 v[44:45], v13 offset0:82 offset1:90
	ds_read2_b32 v[46:47], v13 offset0:115 offset1:123
	ds_read2_b32 v[48:49], v13 offset0:148 offset1:156
	ds_read2_b32 v[50:51], v13 offset0:181 offset1:189
	ds_read2_b32 v[52:53], v13 offset0:214 offset1:222
	ds_read2_b32 v[54:55], v13 offset0:247 offset1:255
	global_store_dwordx4 v[38:39], v[34:37], off
	v_or_b32_e32 v38, 8, v66
	v_mov_b32_e32 v39, v3
	v_lshlrev_b64 v[38:39], 11, v[38:39]
	v_lshl_add_u64 v[38:39], s[4:5], 0, v[38:39]
	v_lshl_add_u64 v[38:39], v[38:39], 0, s[0:1]
	v_lshl_add_u64 v[38:39], v[38:39], 0, v[6:7]
	s_waitcnt lgkmcnt(6)
	v_cvt_pk_bf16_f32 v34, v40, v42
	s_waitcnt lgkmcnt(4)
	v_cvt_pk_bf16_f32 v35, v44, v46
	s_waitcnt lgkmcnt(2)
	v_cvt_pk_bf16_f32 v36, v48, v50
	s_waitcnt lgkmcnt(0)
	v_cvt_pk_bf16_f32 v37, v52, v54
	global_store_dwordx4 v[38:39], v[34:37], off
	v_or_b32_e32 v38, v71, v17
	v_mov_b32_e32 v39, v3
	v_lshlrev_b64 v[38:39], 11, v[38:39]
	v_lshl_add_u64 v[38:39], s[4:5], 0, v[38:39]
	v_lshl_add_u64 v[38:39], v[38:39], 0, s[0:1]
	v_lshl_add_u64 v[38:39], v[38:39], 0, v[6:7]
	v_cvt_pk_bf16_f32 v34, v41, v43
	v_cvt_pk_bf16_f32 v35, v45, v47
	v_cvt_pk_bf16_f32 v36, v49, v51
	v_cvt_pk_bf16_f32 v37, v53, v55
	global_store_dwordx4 v[38:39], v[34:37], off
	s_waitcnt lgkmcnt(0)

; #define GAS __attribute__((address_space(1)))
; #define LAS __attribute__((address_space(3)))
; #define LDS_WAIT() asm volatile("s_waitcnt lgkmcnt(0)" ::: "memory")
; __device__ __forceinline__ unsigned pk2(float lo, float hi) { unsigned r; asm("v_cvt_pk_bf16_f32 %0, %1, %2" : "=v"(r) : "v"(lo), "v"(hi)); return r; }
; __device__ __forceinline__ void titem_load(const TItem& T, int lane, f32x4 (&v)[8]) {
;     const int nblk = T.N / 32, kb = T.item / nblk, nb = T.item % nblk, k0 = 64 * kb, n0 = 32 * nb;
; #pragma unroll
;     for (int i = 0; i < 8; ++i) v[i] = *(const GAS f32x4*)(T.W + (size_t)(k0 + 8 * i + (lane >> 3)) * T.N + n0 + 4 * (lane & 7));
; }
; __device__ __forceinline__ void titem_store(const TItem& T, int lane, const f32x4 (&v)[8], LAS float* scr) {
;     const int nblk = T.N / 32, kb = T.item / nblk, nb = T.item % nblk, k0 = 64 * kb, n0 = 32 * nb;
; #pragma unroll
;     for (int i = 0; i < 8; ++i) { LAS float* s = scr + (8 * i + (lane >> 3)) * 33 + 4 * (lane & 7); s[0] = v[i][0]; s[1] = v[i][1]; s[2] = v[i][2]; s[3] = v[i][3]; }
;     LDS_WAIT(); asm volatile("" ::: "memory");
;     const int c = lane & 7;
; #pragma unroll
;     for (int j = 0; j < 4; ++j) { const int n = (lane >> 3) + 8 * j; const LAS float* s = scr + (8 * c) * 33 + n;
;         if (T.f8) { u32x2 o; o.x = pg8::pack4_fp8(s[0 * 33] * pg8::SC_W, s[1 * 33] * pg8::SC_W, s[2 * 33] * pg8::SC_W, s[3 * 33] * pg8::SC_W); o.y = pg8::pack4_fp8(s[4 * 33] * pg8::SC_W, s[5 * 33] * pg8::SC_W, s[6 * 33] * pg8::SC_W, s[7 * 33] * pg8::SC_W);
;             *(GAS u32x2*)((unsigned char*)T.WT + (size_t)row_map(T.mode, n0, n) * 1024 + k0 + 8 * c) = o; }
;         else { u32x4 o; o.x = pk2(s[0 * 33], s[1 * 33]); o.y = pk2(s[2 * 33], s[3 * 33]); o.z = pk2(s[4 * 33], s[5 * 33]); o.w = pk2(s[6 * 33], s[7 * 33]);
;             *(GAS u32x4*)(T.WT + (size_t)row_map(T.mode, n0, n) * 1024 + k0 + 8 * c) = o; } }
;     LDS_WAIT(); asm volatile("" ::: "memory");
; }
; __device__ __forceinline__ void p0_prologue(const Frame& F0) {
;     ...
;             if (r < I_SQ) { p0_transpose_item(inp(F, I_AWOUT) + (size_t)j * 1024 * 1024, 1024, (bf16_t*)(ws + WS_WAOUT + (size_t)j * 1024 * 1024), RM_P8, scr, r, F.lane, true); continue; } r -= I_SQ;
.LBB0_57:
	s_andn2_b64 vcc, exec, s[4:5]
	s_cbranch_vccnz .LBB0_59
	v_mov_b32_e32 v7, s34
	s_waitcnt vmcnt(0)
	ds_read_b64 v[34:35], v7
	s_and_b64 s[4:5], s[2:3], exec
	s_cselect_b32 s0, 0x100000, 0
	s_lshl_b32 s4, s0, 2
	v_mov_b32_e32 v67, v3
	s_waitcnt lgkmcnt(0)
	v_readfirstlane_b32 s5, v34
	v_readfirstlane_b32 s6, v35
	s_add_u32 s46, s5, s4
	s_addc_u32 s47, s6, 0
	s_add_u32 s4, s13, s0
	s_addc_u32 s5, s16, 0
	s_lshl_b32 s0, s44, 1
	s_add_i32 s0, s0, 0x1fa00
	s_and_b32 s6, s0, 0x1ffc0
	v_or_b32_e32 v7, s6, v70
	s_and_b32 s45, s19, 0x3e0
	v_lshlrev_b32_e32 v34, 12, v7
	v_mov_b32_e32 v35, v3
	v_lshl_add_u64 v[34:35], s[46:47], 0, v[34:35]
	s_lshl_b32 s0, s45, 2
	v_lshl_add_u64 v[34:35], v[34:35], 0, s[0:1]
	v_lshl_add_u64 v[62:63], v[34:35], 0, v[2:3]
	v_add_co_u32_e32 v38, vcc, s35, v62
	v_mov_b32_e32 v66, v3
	s_nop 0
	v_addc_co_u32_e32 v39, vcc, 0, v63, vcc
	v_add_co_u32_e32 v42, vcc, s36, v62
	global_load_dwordx4 v[34:37], v[62:63], off nt
	s_nop 0
	global_load_dwordx4 v[38:41], v[38:39], off nt
	v_addc_co_u32_e32 v43, vcc, 0, v63, vcc
	v_add_co_u32_e32 v46, vcc, s26, v62
	v_or_b32_e32 v7, s45, v1
	s_nop 0
	v_addc_co_u32_e32 v47, vcc, 0, v63, vcc
	v_add_co_u32_e32 v50, vcc, s37, v62
	global_load_dwordx4 v[42:45], v[42:43], off nt
	s_nop 0
	global_load_dwordx4 v[46:49], v[46:47], off nt
	v_addc_co_u32_e32 v51, vcc, 0, v63, vcc
	v_add_co_u32_e32 v54, vcc, s38, v62
	v_or_b32_e32 v68, v7, v14
	s_nop 0
	v_addc_co_u32_e32 v55, vcc, 0, v63, vcc
	global_load_dwordx4 v[50:53], v[50:51], off nt
	s_nop 0
	global_load_dwordx4 v[54:57], v[54:55], off nt
	v_add_co_u32_e32 v58, vcc, s27, v62
	v_mov_b32_e32 v69, v3
	s_nop 0
	v_addc_co_u32_e32 v59, vcc, 0, v63, vcc
	global_load_dwordx4 v[58:61], v[58:59], off nt
	v_add_co_u32_e32 v62, vcc, s39, v62
	v_lshlrev_b32_e32 v68, 10, v68
	s_nop 0
	v_addc_co_u32_e32 v63, vcc, 0, v63, vcc
	global_load_dwordx4 v[62:65], v[62:63], off nt
	s_mov_b32 s7, s1
	v_lshl_add_u64 v[68:69], s[4:5], 0, v[68:69]
	v_lshl_add_u64 v[68:69], v[68:69], 0, s[6:7]
	v_lshl_add_u64 v[68:69], v[68:69], 0, v[4:5]
	s_waitcnt vmcnt(7)
	ds_write2_b32 v18, v34, v35 offset1:1
	ds_write2_b32 v18, v36, v37 offset0:2 offset1:3
	s_waitcnt vmcnt(6)
	ds_write2_b32 v19, v38, v39 offset1:1
	ds_write2_b32 v20, v40, v41 offset1:1
	s_waitcnt vmcnt(5)
	ds_write2_b32 v21, v42, v43 offset1:1
	ds_write2_b32 v22, v44, v45 offset1:1
	s_waitcnt vmcnt(4)
	ds_write2_b32 v23, v46, v47 offset1:1
	ds_write2_b32 v24, v48, v49 offset1:1
	s_waitcnt vmcnt(3)
	ds_write2_b32 v25, v50, v51 offset1:1
	ds_write2_b32 v26, v52, v53 offset1:1
	s_waitcnt vmcnt(2)
	ds_write2_b32 v27, v54, v55 offset1:1
	ds_write2_b32 v28, v56, v57 offset1:1
	s_waitcnt vmcnt(1)
	ds_write2_b32 v29, v58, v59 offset1:1
	ds_write2_b32 v30, v60, v61 offset1:1
	s_waitcnt vmcnt(0)
	ds_write2_b32 v31, v62, v63 offset1:1
	ds_write2_b32 v32, v64, v65 offset1:1
	s_waitcnt lgkmcnt(0)
	ds_read2_b32 v[34:35], v13 offset1:8
	ds_read2_b32 v[36:37], v13 offset0:33 offset1:41
	ds_read2_b32 v[38:39], v13 offset0:66 offset1:74
	ds_read2_b32 v[40:41], v13 offset0:99 offset1:107
	ds_read2_b32 v[42:43], v13 offset0:132 offset1:140
	ds_read2_b32 v[44:45], v13 offset0:165 offset1:173
	ds_read2_b32 v[46:47], v13 offset0:198 offset1:206
	ds_read2_b32 v[48:49], v13 offset0:231 offset1:239
	s_waitcnt lgkmcnt(7)
	v_mul_f32_e32 v34, 0x43800000, v34
	s_waitcnt lgkmcnt(3)
	v_mul_f32_e32 v42, 0x43800000, v42
	s_waitcnt lgkmcnt(2)
	v_mul_f32_e32 v44, 0x43800000, v44
	v_med3_f32 v42, v42, s40, v33
	v_med3_f32 v44, v44, s40, v33
	v_cvt_pk_fp8_f32 v67, v42, v44
	v_mul_f32_e32 v36, 0x43800000, v36
	s_waitcnt lgkmcnt(1)
	v_mul_f32_e32 v46, 0x43800000, v46
	s_waitcnt lgkmcnt(0)
; #define GAS __attribute__((address_space(1)))
; #define LAS __attribute__((address_space(3)))
; #define LDS_WAIT() asm volatile("s_waitcnt lgkmcnt(0)" ::: "memory")
; __device__ __forceinline__ unsigned pk2(float lo, float hi) { unsigned r; asm("v_cvt_pk_bf16_f32 %0, %1, %2" : "=v"(r) : "v"(lo), "v"(hi)); return r; }
; __device__ __forceinline__ float clamp448(float x) { return __builtin_fminf(__builtin_fmaxf(x, -448.f), 448.f); }
; __device__ __forceinline__ unsigned pack4_fp8(float a, float b, float c, float d) {
;     int p = __builtin_amdgcn_cvt_pk_fp8_f32(clamp448(a), clamp448(b), 0, false); p = __builtin_amdgcn_cvt_pk_fp8_f32(clamp448(c), clamp448(d), p, true); return (unsigned)p; }
; __device__ __forceinline__ void titem_store(const TItem& T, int lane, const f32x4 (&v)[8], LAS float* scr) {
;     const int nblk = T.N / 32, kb = T.item / nblk, nb = T.item % nblk, k0 = 64 * kb, n0 = 32 * nb;
; #pragma unroll
;     for (int i = 0; i < 8; ++i) { LAS float* s = scr + (8 * i + (lane >> 3)) * 33 + 4 * (lane & 7); s[0] = v[i][0]; s[1] = v[i][1]; s[2] = v[i][2]; s[3] = v[i][3]; }
;     LDS_WAIT(); asm volatile("" ::: "memory");
;     const int c = lane & 7;
; #pragma unroll
;     for (int j = 0; j < 4; ++j) { const int n = (lane >> 3) + 8 * j; const LAS float* s = scr + (8 * c) * 33 + n;
;         if (T.f8) { u32x2 o; o.x = pg8::pack4_fp8(s[0 * 33] * pg8::SC_W, s[1 * 33] * pg8::SC_W, s[2 * 33] * pg8::SC_W, s[3 * 33] * pg8::SC_W); o.y = pg8::pack4_fp8(s[4 * 33] * pg8::SC_W, s[5 * 33] * pg8::SC_W, s[6 * 33] * pg8::SC_W, s[7 * 33] * pg8::SC_W);
;             *(GAS u32x2*)((unsigned char*)T.WT + (size_t)row_map(T.mode, n0, n) * 1024 + k0 + 8 * c) = o; }
;         else { u32x4 o; o.x = pk2(s[0 * 33], s[1 * 33]); o.y = pk2(s[2 * 33], s[3 * 33]); o.z = pk2(s[4 * 33], s[5 * 33]); o.w = pk2(s[6 * 33], s[7 * 33]);
;             *(GAS u32x4*)(T.WT + (size_t)row_map(T.mode, n0, n) * 1024 + k0 + 8 * c) = o; } }
;     LDS_WAIT(); asm volatile("" ::: "memory");
; }
	v_mul_f32_e32 v48, 0x43800000, v48
	v_med3_f32 v34, v34, s40, v33
	v_med3_f32 v36, v36, s40, v33
	v_cvt_pk_fp8_f32 v66, v34, v36
	v_med3_f32 v34, v46, s40, v33
	v_med3_f32 v36, v48, s40, v33
	v_cvt_pk_fp8_f32 v67, v34, v36 op_sel:[0,0,1]
	v_mul_f32_e32 v34, 0x43800000, v35
	v_mul_f32_e32 v35, 0x43800000, v37
	v_mul_f32_e32 v38, 0x43800000, v38
	v_mul_f32_e32 v40, 0x43800000, v40
	v_med3_f32 v37, v34, s40, v33
	v_med3_f32 v35, v35, s40, v33
	v_mov_b32_e32 v34, v3
	v_med3_f32 v38, v38, s40, v33
	v_med3_f32 v40, v40, s40, v33
	v_cvt_pk_fp8_f32 v34, v37, v35
	v_cvt_pk_fp8_f32 v66, v38, v40 op_sel:[0,0,1]
	v_mul_f32_e32 v36, 0x43800000, v39
	v_mul_f32_e32 v35, 0x43800000, v41
	v_med3_f32 v36, v36, s40, v33
	v_med3_f32 v35, v35, s40, v33
	v_cvt_pk_fp8_f32 v34, v36, v35 op_sel:[0,0,1]
	v_mul_f32_e32 v35, 0x43800000, v43
	v_mul_f32_e32 v36, 0x43800000, v45
	global_store_dwordx2 v[68:69], v[66:67], off
	v_mul_f32_e32 v37, 0x43800000, v47
	v_mul_f32_e32 v38, 0x43800000, v49
	v_med3_f32 v39, v35, s40, v33
	v_med3_f32 v36, v36, s40, v33
	v_mov_b32_e32 v35, v3
	v_cvt_pk_fp8_f32 v35, v39, v36
	v_med3_f32 v44, v37, s40, v33
	v_med3_f32 v45, v38, s40, v33
	ds_read2_b32 v[36:37], v13 offset0:16 offset1:24
	ds_read2_b32 v[38:39], v13 offset0:49 offset1:57
	ds_read2_b32 v[40:41], v13 offset0:82 offset1:90
	ds_read2_b32 v[42:43], v13 offset0:115 offset1:123
	v_cvt_pk_fp8_f32 v35, v44, v45 op_sel:[0,0,1]
	s_waitcnt lgkmcnt(3)
	v_mul_f32_e32 v36, 0x43800000, v36
	s_waitcnt lgkmcnt(2)
	v_mul_f32_e32 v38, 0x43800000, v38
	v_med3_f32 v36, v36, s40, v33
	v_med3_f32 v38, v38, s40, v33
	v_mov_b32_e32 v44, v3
	v_cvt_pk_fp8_f32 v44, v36, v38
	ds_read2_b32 v[46:47], v13 offset0:148 offset1:156
	ds_read2_b32 v[48:49], v13 offset0:181 offset1:189
	ds_read2_b32 v[50:51], v13 offset0:214 offset1:222
	s_waitcnt lgkmcnt(4)
	v_mul_f32_e32 v40, 0x43800000, v40
	s_waitcnt lgkmcnt(3)
	v_mul_f32_e32 v42, 0x43800000, v42
	v_med3_f32 v36, v40, s40, v33
	v_med3_f32 v38, v42, s40, v33
	ds_read2_b32 v[52:53], v13 offset0:247 offset1:255
	v_cvt_pk_fp8_f32 v44, v36, v38 op_sel:[0,0,1]
	s_waitcnt lgkmcnt(3)
	v_mul_f32_e32 v36, 0x43800000, v46
	s_waitcnt lgkmcnt(2)
	v_mul_f32_e32 v38, 0x43800000, v48
	v_med3_f32 v36, v36, s40, v33
	v_med3_f32 v38, v38, s40, v33
	v_mov_b32_e32 v45, v3
	v_cvt_pk_fp8_f32 v45, v36, v38
	s_waitcnt lgkmcnt(1)
	v_mul_f32_e32 v40, 0x43800000, v50
	s_waitcnt lgkmcnt(0)
	v_mul_f32_e32 v36, 0x43800000, v52
	v_med3_f32 v38, v40, s40, v33
	v_med3_f32 v36, v36, s40, v33
	v_cvt_pk_fp8_f32 v45, v38, v36 op_sel:[0,0,1]
	v_add_co_u32_e32 v54, vcc, s22, v68
	v_mul_f32_e32 v36, 0x43800000, v41
	s_nop 0
	v_addc_co_u32_e32 v55, vcc, 0, v69, vcc
	global_store_dwordx2 v[54:55], v[34:35], off offset:-4096
	global_store_dwordx2 v[54:55], v[44:45], off
	v_mul_f32_e32 v34, 0x43800000, v37
	v_mul_f32_e32 v35, 0x43800000, v39
	v_med3_f32 v37, v34, s40, v33
	v_med3_f32 v35, v35, s40, v33
	v_mov_b32_e32 v34, v3
	v_cvt_pk_fp8_f32 v34, v37, v35
	v_mul_f32_e32 v35, 0x43800000, v43
	v_med3_f32 v36, v36, s40, v33
	v_med3_f32 v35, v35, s40, v33
	v_cvt_pk_fp8_f32 v34, v36, v35 op_sel:[0,0,1]
	v_mul_f32_e32 v35, 0x43800000, v47
	v_mul_f32_e32 v36, 0x43800000, v49
	v_med3_f32 v38, v35, s40, v33
	v_med3_f32 v36, v36, s40, v33
	v_mov_b32_e32 v35, v3
	v_cvt_pk_fp8_f32 v35, v38, v36
	v_mul_f32_e32 v37, 0x43800000, v51
	v_mul_f32_e32 v36, 0x43800000, v53
	v_med3_f32 v37, v37, s40, v33
	v_med3_f32 v36, v36, s40, v33
	v_cvt_pk_fp8_f32 v35, v37, v36 op_sel:[0,0,1]
	v_lshl_or_b32 v36, v7, 10, v16
	v_mov_b32_e32 v37, v3
	v_lshl_add_u64 v[36:37], s[4:5], 0, v[36:37]
	v_lshl_add_u64 v[36:37], v[36:37], 0, s[6:7]
	v_lshl_add_u64 v[36:37], v[36:37], 0, v[4:5]
	global_store_dwordx2 v[36:37], v[34:35], off
	s_waitcnt lgkmcnt(0)

; #define GAS __attribute__((address_space(1)))
; #define LAS __attribute__((address_space(3)))
; #define LDS_WAIT() asm volatile("s_waitcnt lgkmcnt(0)" ::: "memory")
; __device__ __forceinline__ unsigned pk2(float lo, float hi) { unsigned r; asm("v_cvt_pk_bf16_f32 %0, %1, %2" : "=v"(r) : "v"(lo), "v"(hi)); return r; }
; __device__ __forceinline__ void titem_load(const TItem& T, int lane, f32x4 (&v)[8]) {
;     const int nblk = T.N / 32, kb = T.item / nblk, nb = T.item % nblk, k0 = 64 * kb, n0 = 32 * nb;
; #pragma unroll
;     for (int i = 0; i < 8; ++i) v[i] = *(const GAS f32x4*)(T.W + (size_t)(k0 + 8 * i + (lane >> 3)) * T.N + n0 + 4 * (lane & 7));
; }
; __device__ __forceinline__ void titem_store(const TItem& T, int lane, const f32x4 (&v)[8], LAS float* scr) {
;     const int nblk = T.N / 32, kb = T.item / nblk, nb = T.item % nblk, k0 = 64 * kb, n0 = 32 * nb;
; #pragma unroll
;     for (int i = 0; i < 8; ++i) { LAS float* s = scr + (8 * i + (lane >> 3)) * 33 + 4 * (lane & 7); s[0] = v[i][0]; s[1] = v[i][1]; s[2] = v[i][2]; s[3] = v[i][3]; }
;     LDS_WAIT(); asm volatile("" ::: "memory");
;     const int c = lane & 7;
; #pragma unroll
;     for (int j = 0; j < 4; ++j) { const int n = (lane >> 3) + 8 * j; const LAS float* s = scr + (8 * c) * 33 + n;
;         if (T.f8) { u32x2 o; o.x = pg8::pack4_fp8(s[0 * 33] * pg8::SC_W, s[1 * 33] * pg8::SC_W, s[2 * 33] * pg8::SC_W, s[3 * 33] * pg8::SC_W); o.y = pg8::pack4_fp8(s[4 * 33] * pg8::SC_W, s[5 * 33] * pg8::SC_W, s[6 * 33] * pg8::SC_W, s[7 * 33] * pg8::SC_W);
;             *(GAS u32x2*)((unsigned char*)T.WT + (size_t)row_map(T.mode, n0, n) * 1024 + k0 + 8 * c) = o; }
;         else { u32x4 o; o.x = pk2(s[0 * 33], s[1 * 33]); o.y = pk2(s[2 * 33], s[3 * 33]); o.z = pk2(s[4 * 33], s[5 * 33]); o.w = pk2(s[6 * 33], s[7 * 33]);
;             *(GAS u32x4*)(T.WT + (size_t)row_map(T.mode, n0, n) * 1024 + k0 + 8 * c) = o; } }
;     LDS_WAIT(); asm volatile("" ::: "memory");
; }
; __device__ __forceinline__ void p0_prologue(const Frame& F0) {
;     ...
;             if (r < I_AIN) { p0_transpose_item(inp(F, I_AWIN) + (size_t)j * 1024 * 1536, 1536, (bf16_t*)(ws + WS_WAIN + (size_t)j * 1536 * 1024), RM_AIN, scr, r, F.lane, true); continue; } r -= I_AIN;
.LBB0_61:
	v_mov_b32_e32 v7, s41
	s_waitcnt vmcnt(0)
	ds_read_b64 v[34:35], v7
	s_and_b64 s[2:3], s[2:3], exec
	s_cselect_b32 s0, 0x180000, 0
	s_lshl_b32 s2, s0, 2
	v_mov_b32_e32 v66, v3
	s_waitcnt lgkmcnt(0)
	v_readfirstlane_b32 s3, v34
	v_readfirstlane_b32 s4, v35
	s_add_u32 s6, s3, s2
	s_addc_u32 s7, s4, 0
	s_add_u32 s2, s17, s0
	s_mul_hi_i32 s0, s44, 0x2aaaaaab
	s_addc_u32 s3, s18, 0
	s_lshr_b32 s4, s0, 31
	s_ashr_i32 s0, s0, 3
	s_add_i32 s0, s0, s4
	s_mul_i32 s4, s0, 48
	s_sub_i32 s48, s44, s4
	s_lshl_b32 s4, s0, 6
	s_lshl_b32 s44, s48, 5
	v_or_b32_e32 v7, s4, v70
	v_mov_b64_e32 v[62:63], s[6:7]
	s_ashr_i32 s45, s44, 31
	v_mad_i64_i32 v[34:35], s[6:7], v7, s42, v[62:63]
	v_or_b32_e32 v36, 8, v7
	v_or_b32_e32 v42, 16, v7
	v_or_b32_e32 v44, 24, v7
	v_or_b32_e32 v50, 32, v7
	v_or_b32_e32 v52, 40, v7
	s_lshl_b64 s[6:7], s[44:45], 2
	v_mad_i64_i32 v[36:37], s[46:47], v36, s42, v[62:63]
	v_mad_i64_i32 v[42:43], s[46:47], v42, s42, v[62:63]
	v_mad_i64_i32 v[44:45], s[46:47], v44, s42, v[62:63]
	v_mad_i64_i32 v[50:51], s[46:47], v50, s42, v[62:63]
	v_mad_i64_i32 v[52:53], s[46:47], v52, s42, v[62:63]
	v_lshl_add_u64 v[34:35], v[34:35], 0, s[6:7]
	v_lshl_add_u64 v[36:37], v[36:37], 0, s[6:7]
	v_lshl_add_u64 v[42:43], v[42:43], 0, s[6:7]
	v_lshl_add_u64 v[44:45], v[44:45], 0, s[6:7]
	v_lshl_add_u64 v[50:51], v[50:51], 0, s[6:7]
	v_lshl_add_u64 v[52:53], v[52:53], 0, s[6:7]
	v_lshl_add_u64 v[34:35], v[34:35], 0, v[2:3]
	v_lshl_add_u64 v[38:39], v[36:37], 0, v[2:3]
	v_lshl_add_u64 v[42:43], v[42:43], 0, v[2:3]
	v_lshl_add_u64 v[46:47], v[44:45], 0, v[2:3]
	v_lshl_add_u64 v[50:51], v[50:51], 0, v[2:3]
	v_lshl_add_u64 v[54:55], v[52:53], 0, v[2:3]
	global_load_dwordx4 v[34:37], v[34:35], off nt
	s_nop 0
	global_load_dwordx4 v[38:41], v[38:39], off nt
	s_nop 0
	global_load_dwordx4 v[42:45], v[42:43], off nt
	s_nop 0
	global_load_dwordx4 v[46:49], v[46:47], off nt
	s_nop 0
	global_load_dwordx4 v[50:53], v[50:51], off nt
	s_nop 0
	global_load_dwordx4 v[54:57], v[54:55], off nt
	v_or_b32_e32 v58, 48, v7
	v_mad_i64_i32 v[58:59], s[46:47], v58, s42, v[62:63]
	v_lshl_add_u64 v[58:59], v[58:59], 0, s[6:7]
	v_or_b32_e32 v7, 56, v7
	v_lshl_add_u64 v[58:59], v[58:59], 0, v[2:3]
	v_mad_i64_i32 v[62:63], s[46:47], v7, s42, v[62:63]
	global_load_dwordx4 v[58:61], v[58:59], off nt
	v_lshl_add_u64 v[62:63], v[62:63], 0, s[6:7]
	v_lshl_add_u64 v[62:63], v[62:63], 0, v[2:3]
	global_load_dwordx4 v[62:65], v[62:63], off nt
	v_mov_b32_e32 v67, v3
	s_lshl_b32 s0, s48, 7
	s_lshl_b32 s6, s48, 4
	s_and_b32 s7, s44, 0xffffff00
	s_and_b32 s0, s0, 0x80
	s_and_b32 s6, s6, 0x60
	s_or_b32 s0, s7, s0
	s_or_b32 s0, s0, s6
	s_ashr_i32 s5, s4, 31
	s_waitcnt vmcnt(7)
	ds_write2_b32 v18, v34, v35 offset1:1
	ds_write2_b32 v18, v36, v37 offset0:2 offset1:3
	s_waitcnt vmcnt(6)
	ds_write2_b32 v19, v38, v39 offset1:1
	ds_write2_b32 v20, v40, v41 offset1:1
	s_waitcnt vmcnt(5)
	ds_write2_b32 v21, v42, v43 offset1:1
	ds_write2_b32 v22, v44, v45 offset1:1
	s_waitcnt vmcnt(4)
	ds_write2_b32 v23, v46, v47 offset1:1
	ds_write2_b32 v24, v48, v49 offset1:1
	s_waitcnt vmcnt(3)
	ds_write2_b32 v25, v50, v51 offset1:1
	ds_write2_b32 v26, v52, v53 offset1:1
	s_waitcnt vmcnt(2)
	ds_write2_b32 v27, v54, v55 offset1:1
	ds_write2_b32 v28, v56, v57 offset1:1
	s_waitcnt vmcnt(1)
	ds_write2_b32 v29, v58, v59 offset1:1
	ds_write2_b32 v30, v60, v61 offset1:1
	s_waitcnt vmcnt(0)
	ds_write2_b32 v31, v62, v63 offset1:1
	ds_write2_b32 v32, v64, v65 offset1:1
	s_waitcnt lgkmcnt(0)
	ds_read2_b32 v[34:35], v13 offset1:8
	ds_read2_b32 v[36:37], v13 offset0:33 offset1:41
	ds_read2_b32 v[38:39], v13 offset0:66 offset1:74
	ds_read2_b32 v[40:41], v13 offset0:99 offset1:107
	ds_read2_b32 v[42:43], v13 offset0:132 offset1:140
	ds_read2_b32 v[44:45], v13 offset0:165 offset1:173
	ds_read2_b32 v[46:47], v13 offset0:198 offset1:206
	s_waitcnt lgkmcnt(6)
	v_mul_f32_e32 v7, 0x43800000, v34
	s_waitcnt lgkmcnt(5)
	v_mul_f32_e32 v34, 0x43800000, v36
	v_med3_f32 v7, v7, s40, v33
	v_med3_f32 v34, v34, s40, v33
	v_cvt_pk_fp8_f32 v66, v7, v34
	s_waitcnt lgkmcnt(4)
	v_mul_f32_e32 v36, 0x43800000, v38
	s_waitcnt lgkmcnt(3)
	v_mul_f32_e32 v7, 0x43800000, v40
	v_med3_f32 v34, v36, s40, v33
	v_med3_f32 v7, v7, s40, v33
	ds_read2_b32 v[48:49], v13 offset0:231 offset1:239
	v_cvt_pk_fp8_f32 v66, v34, v7 op_sel:[0,0,1]
	s_waitcnt lgkmcnt(3)
; #define GAS __attribute__((address_space(1)))
; #define LAS __attribute__((address_space(3)))
; #define LDS_WAIT() asm volatile("s_waitcnt lgkmcnt(0)" ::: "memory")
; __device__ __forceinline__ unsigned pk2(float lo, float hi) { unsigned r; asm("v_cvt_pk_bf16_f32 %0, %1, %2" : "=v"(r) : "v"(lo), "v"(hi)); return r; }
; __device__ __forceinline__ void titem_store(const TItem& T, int lane, const f32x4 (&v)[8], LAS float* scr) {
;     const int nblk = T.N / 32, kb = T.item / nblk, nb = T.item % nblk, k0 = 64 * kb, n0 = 32 * nb;
; #pragma unroll
;     for (int i = 0; i < 8; ++i) { LAS float* s = scr + (8 * i + (lane >> 3)) * 33 + 4 * (lane & 7); s[0] = v[i][0]; s[1] = v[i][1]; s[2] = v[i][2]; s[3] = v[i][3]; }
;     LDS_WAIT(); asm volatile("" ::: "memory");
;     const int c = lane & 7;
; #pragma unroll
;     for (int j = 0; j < 4; ++j) { const int n = (lane >> 3) + 8 * j; const LAS float* s = scr + (8 * c) * 33 + n;
;         if (T.f8) { u32x2 o; o.x = pg8::pack4_fp8(s[0 * 33] * pg8::SC_W, s[1 * 33] * pg8::SC_W, s[2 * 33] * pg8::SC_W, s[3 * 33] * pg8::SC_W); o.y = pg8::pack4_fp8(s[4 * 33] * pg8::SC_W, s[5 * 33] * pg8::SC_W, s[6 * 33] * pg8::SC_W, s[7 * 33] * pg8::SC_W);
;             *(GAS u32x2*)((unsigned char*)T.WT + (size_t)row_map(T.mode, n0, n) * 1024 + k0 + 8 * c) = o; }
;         else { u32x4 o; o.x = pk2(s[0 * 33], s[1 * 33]); o.y = pk2(s[2 * 33], s[3 * 33]); o.z = pk2(s[4 * 33], s[5 * 33]); o.w = pk2(s[6 * 33], s[7 * 33]);
;             *(GAS u32x4*)(T.WT + (size_t)row_map(T.mode, n0, n) * 1024 + k0 + 8 * c) = o; } }
;     LDS_WAIT(); asm volatile("" ::: "memory");
; }
; __device__ __forceinline__ void p0_prologue(const Frame& F0) {
;     ...
;         for (int it = gw; it < NITEMS; it += NGW) {
;             if (it >= NSMALL) break;
;             int r = it; const int j = r >= NSMALL / 2 ? 1 : 0; r -= j * (NSMALL / 2);
;             if (r < I_AIN) { p0_transpose_item(inp(F, I_AWIN) + (size_t)j * 1024 * 1536, 1536, (bf16_t*)(ws + WS_WAIN + (size_t)j * 1536 * 1024), RM_AIN, scr, r, F.lane, true); continue; } r -= I_AIN;
	v_mul_f32_e32 v7, 0x43800000, v42
	s_waitcnt lgkmcnt(2)
	v_mul_f32_e32 v34, 0x43800000, v44
	v_med3_f32 v7, v7, s40, v33
	v_med3_f32 v34, v34, s40, v33
	v_cvt_pk_fp8_f32 v67, v7, v34
	s_waitcnt lgkmcnt(1)
	v_mul_f32_e32 v36, 0x43800000, v46
	s_waitcnt lgkmcnt(0)
	v_mul_f32_e32 v7, 0x43800000, v48
	v_med3_f32 v34, v36, s40, v33
	v_med3_f32 v7, v7, s40, v33
	v_cvt_pk_fp8_f32 v67, v34, v7 op_sel:[0,0,1]
	v_mul_f32_e32 v7, 0x43800000, v35
	v_mul_f32_e32 v34, 0x43800000, v37
	v_med3_f32 v7, v7, s40, v33
	v_med3_f32 v36, v34, s40, v33
	v_mov_b32_e32 v34, v3
	v_cvt_pk_fp8_f32 v34, v7, v36
	v_mul_f32_e32 v35, 0x43800000, v39
	v_mul_f32_e32 v7, 0x43800000, v41
	v_med3_f32 v35, v35, s40, v33
	v_med3_f32 v7, v7, s40, v33
	v_cvt_pk_fp8_f32 v34, v35, v7 op_sel:[0,0,1]
	v_mul_f32_e32 v7, 0x43800000, v43
	v_mul_f32_e32 v35, 0x43800000, v45
	v_med3_f32 v7, v7, s40, v33
	v_med3_f32 v37, v35, s40, v33
	v_mov_b32_e32 v35, v3
	v_or_b32_e32 v50, s0, v70
	v_cvt_pk_fp8_f32 v35, v7, v37
	v_ashrrev_i32_e32 v51, 31, v50
	v_lshlrev_b64 v[50:51], 10, v[50:51]
	v_mul_f32_e32 v36, 0x43800000, v47
	v_mul_f32_e32 v7, 0x43800000, v49
	v_lshl_add_u64 v[50:51], s[2:3], 0, v[50:51]
	v_med3_f32 v36, v36, s40, v33
	v_med3_f32 v7, v7, s40, v33
	v_lshl_add_u64 v[50:51], v[50:51], 0, s[4:5]
	v_cvt_pk_fp8_f32 v35, v36, v7 op_sel:[0,0,1]
	v_or_b32_e32 v36, s0, v10
	v_lshl_add_u64 v[50:51], v[50:51], 0, v[4:5]
	v_ashrrev_i32_e32 v37, 31, v36
	global_store_dwordx2 v[50:51], v[66:67], off
	v_lshlrev_b64 v[36:37], 10, v[36:37]
	v_lshl_add_u64 v[36:37], s[2:3], 0, v[36:37]
	ds_read2_b32 v[38:39], v13 offset0:16 offset1:24
	ds_read2_b32 v[40:41], v13 offset0:49 offset1:57
	ds_read2_b32 v[42:43], v13 offset0:82 offset1:90
	ds_read2_b32 v[44:45], v13 offset0:115 offset1:123
	v_lshl_add_u64 v[36:37], v[36:37], 0, s[4:5]
	v_lshl_add_u64 v[36:37], v[36:37], 0, v[4:5]
	global_store_dwordx2 v[36:37], v[34:35], off
	s_waitcnt lgkmcnt(3)
	v_mul_f32_e32 v7, 0x43800000, v38
	s_waitcnt lgkmcnt(2)
	v_mul_f32_e32 v34, 0x43800000, v40
	v_med3_f32 v7, v7, s40, v33
	v_med3_f32 v36, v34, s40, v33
	v_mov_b32_e32 v34, v3
	v_cvt_pk_fp8_f32 v34, v7, v36
	ds_read2_b32 v[36:37], v13 offset0:148 offset1:156
	ds_read2_b32 v[46:47], v13 offset0:181 offset1:189
	ds_read2_b32 v[48:49], v13 offset0:214 offset1:222
	s_waitcnt lgkmcnt(4)
	v_mul_f32_e32 v35, 0x43800000, v42
	s_waitcnt lgkmcnt(3)
	v_mul_f32_e32 v38, 0x43800000, v44
	v_med3_f32 v7, v35, s40, v33
	v_med3_f32 v35, v38, s40, v33
	ds_read2_b32 v[50:51], v13 offset0:247 offset1:255
	v_cvt_pk_fp8_f32 v34, v7, v35 op_sel:[0,0,1]
	s_waitcnt lgkmcnt(3)
	v_mul_f32_e32 v7, 0x43800000, v36
	s_waitcnt lgkmcnt(2)
	v_mul_f32_e32 v35, 0x43800000, v46
	v_med3_f32 v7, v7, s40, v33
	v_med3_f32 v38, v35, s40, v33
	v_mov_b32_e32 v35, v3
	v_cvt_pk_fp8_f32 v35, v7, v38
	s_waitcnt lgkmcnt(1)
	v_mul_f32_e32 v36, 0x43800000, v48
	s_waitcnt lgkmcnt(0)
	v_mul_f32_e32 v7, 0x43800000, v50
	v_or_b32_e32 v52, s0, v11
	v_med3_f32 v36, v36, s40, v33
	v_med3_f32 v7, v7, s40, v33
	v_ashrrev_i32_e32 v53, 31, v52
	v_cvt_pk_fp8_f32 v35, v36, v7 op_sel:[0,0,1]
	v_lshlrev_b64 v[52:53], 10, v[52:53]
	v_lshl_add_u64 v[52:53], s[2:3], 0, v[52:53]
	v_lshl_add_u64 v[52:53], v[52:53], 0, s[4:5]
	v_lshl_add_u64 v[52:53], v[52:53], 0, v[4:5]
	global_store_dwordx2 v[52:53], v[34:35], off
	v_mul_f32_e32 v7, 0x43800000, v39
	v_mul_f32_e32 v34, 0x43800000, v41
	v_med3_f32 v7, v7, s40, v33
	v_med3_f32 v36, v34, s40, v33
	v_mov_b32_e32 v34, v3
	v_cvt_pk_fp8_f32 v34, v7, v36
	v_mul_f32_e32 v35, 0x43800000, v43
	v_mul_f32_e32 v7, 0x43800000, v45
	v_med3_f32 v35, v35, s40, v33
	v_med3_f32 v7, v7, s40, v33
	v_cvt_pk_fp8_f32 v34, v35, v7 op_sel:[0,0,1]
	v_mul_f32_e32 v7, 0x43800000, v37
	v_mul_f32_e32 v35, 0x43800000, v47
	v_med3_f32 v7, v7, s40, v33
	v_med3_f32 v37, v35, s40, v33
	v_mov_b32_e32 v35, v3
	v_cvt_pk_fp8_f32 v35, v7, v37
	v_mul_f32_e32 v36, 0x43800000, v49
	v_mul_f32_e32 v7, 0x43800000, v51
	v_med3_f32 v36, v36, s40, v33
	v_med3_f32 v7, v7, s40, v33
	v_cvt_pk_fp8_f32 v35, v36, v7 op_sel:[0,0,1]
	v_or_b32_e32 v36, s0, v12
	v_ashrrev_i32_e32 v37, 31, v36
	v_lshlrev_b64 v[36:37], 10, v[36:37]
	v_lshl_add_u64 v[36:37], s[2:3], 0, v[36:37]
	v_lshl_add_u64 v[36:37], v[36:37], 0, s[4:5]
	v_lshl_add_u64 v[36:37], v[36:37], 0, v[4:5]
	global_store_dwordx2 v[36:37], v[34:35], off
	s_waitcnt lgkmcnt(0)
	s_branch .LBB0_49

; #define GAS __attribute__((address_space(1)))
; #define LAS __attribute__((address_space(3)))
; #define LDS_WAIT() asm volatile("s_waitcnt lgkmcnt(0)" ::: "memory")
; __device__ __forceinline__ void titem_load(const TItem& T, int lane, f32x4 (&v)[8]) {
;     const int nblk = T.N / 32, kb = T.item / nblk, nb = T.item % nblk, k0 = 64 * kb, n0 = 32 * nb;
; #pragma unroll
;     for (int i = 0; i < 8; ++i) v[i] = *(const GAS f32x4*)(T.W + (size_t)(k0 + 8 * i + (lane >> 3)) * T.N + n0 + 4 * (lane & 7));
; }
; __device__ __forceinline__ void titem_store(const TItem& T, int lane, const f32x4 (&v)[8], LAS float* scr) {
;     const int nblk = T.N / 32, kb = T.item / nblk, nb = T.item % nblk, k0 = 64 * kb, n0 = 32 * nb;
; #pragma unroll
;     for (int i = 0; i < 8; ++i) { LAS float* s = scr + (8 * i + (lane >> 3)) * 33 + 4 * (lane & 7); s[0] = v[i][0]; s[1] = v[i][1]; s[2] = v[i][2]; s[3] = v[i][3]; }
;     LDS_WAIT(); asm volatile("" ::: "memory");
;     const int c = lane & 7;
; #pragma unroll
;     for (int j = 0; j < 4; ++j) { const int n = (lane >> 3) + 8 * j; const LAS float* s = scr + (8 * c) * 33 + n;
;         if (T.f8) { u32x2 o; o.x = pg8::pack4_fp8(s[0 * 33] * pg8::SC_W, s[1 * 33] * pg8::SC_W, s[2 * 33] * pg8::SC_W, s[3 * 33] * pg8::SC_W); o.y = pg8::pack4_fp8(s[4 * 33] * pg8::SC_W, s[5 * 33] * pg8::SC_W, s[6 * 33] * pg8::SC_W, s[7 * 33] * pg8::SC_W);
;             *(GAS u32x2*)((unsigned char*)T.WT + (size_t)row_map(T.mode, n0, n) * 1024 + k0 + 8 * c) = o; }
;         else { u32x4 o; o.x = pk2(s[0 * 33], s[1 * 33]); o.y = pk2(s[2 * 33], s[3 * 33]); o.z = pk2(s[4 * 33], s[5 * 33]); o.w = pk2(s[6 * 33], s[7 * 33]);
;             *(GAS u32x4*)(T.WT + (size_t)row_map(T.mode, n0, n) * 1024 + k0 + 8 * c) = o; } }
;     LDS_WAIT(); asm volatile("" ::: "memory");
; }
; __device__ __forceinline__ void moe_convert_run(Frame& F, int L, int first, int end, int stride, LAS float* scr) {
;     if (first >= end) return;
;     f32x4 nv[8]; TItem nT = moe_item(F, L, first); titem_load(nT, F.lane, nv);
;     for (int r = first; r < end; r += stride) {
;         const TItem T = nT; f32x4 v[8];
; #pragma unroll
;         for (int i = 0; i < 8; ++i) v[i] = nv[i];
;         if (r + stride < end) { nT = moe_item(F, L, r + stride); titem_load(nT, F.lane, nv); }
;         titem_store(T, F.lane, v, scr);
;     }
; }
.LBB0_75:
	s_lshl_b64 s[4:5], s[4:5], 2
	s_add_u32 s4, s13, s4
	s_addc_u32 s5, s16, s5
	s_lshl_b32 s6, s11, 9
	s_sub_i32 s11, s14, s6
	s_bfe_u32 s6, s11, 0x5001a
	s_add_i32 s6, s11, s6
	s_sext_i32_i16 s7, s6
	s_lshl_b32 s7, s7, 1
	s_andn2_b32 s7, s7, 63
	s_and_b32 s6, s6, 0xffe0
	v_or_b32_e32 v2, s7, v70
	s_sub_i32 s6, s11, s6
	s_sext_i32_i16 s6, s6
	v_or_b32_e32 v20, 8, v2
	s_lshl_b32 s6, s6, 5
	v_or_b32_e32 v10, 48, v2
	v_or_b32_e32 v12, 40, v2
	v_or_b32_e32 v14, 32, v2
	v_or_b32_e32 v16, 24, v2
	v_or_b32_e32 v18, 16, v2
	v_ashrrev_i32_e32 v21, 31, v20
	v_ashrrev_i32_e32 v3, 31, v2
	v_or_b32_e32 v4, 56, v2
	s_ashr_i32 s7, s6, 31
	v_ashrrev_i32_e32 v11, 31, v10
	v_ashrrev_i32_e32 v13, 31, v12
	v_ashrrev_i32_e32 v15, 31, v14
	v_ashrrev_i32_e32 v17, 31, v16
	v_ashrrev_i32_e32 v19, 31, v18
	v_lshlrev_b64 v[20:21], 12, v[20:21]
	v_lshlrev_b64 v[2:3], 12, v[2:3]
	v_ashrrev_i32_e32 v5, 31, v4
	s_lshl_b64 s[6:7], s[6:7], 2
	v_and_b32_e32 v6, 28, v9
	v_lshlrev_b64 v[10:11], 12, v[10:11]
	v_lshlrev_b64 v[12:13], 12, v[12:13]
	v_lshlrev_b64 v[14:15], 12, v[14:15]
	v_lshlrev_b64 v[16:17], 12, v[16:17]
	v_lshlrev_b64 v[18:19], 12, v[18:19]
	v_lshl_add_u64 v[20:21], s[4:5], 0, v[20:21]
	v_lshl_add_u64 v[2:3], s[4:5], 0, v[2:3]
	v_lshlrev_b64 v[4:5], 12, v[4:5]
	v_mov_b32_e32 v67, 0
	v_lshlrev_b32_e32 v66, 2, v6
	v_lshl_add_u64 v[10:11], s[4:5], 0, v[10:11]
	v_lshl_add_u64 v[12:13], s[4:5], 0, v[12:13]
	v_lshl_add_u64 v[14:15], s[4:5], 0, v[14:15]
	v_lshl_add_u64 v[16:17], s[4:5], 0, v[16:17]
	v_lshl_add_u64 v[18:19], s[4:5], 0, v[18:19]
	v_lshl_add_u64 v[20:21], v[20:21], 0, s[6:7]
	v_lshl_add_u64 v[2:3], v[2:3], 0, s[6:7]
	v_lshl_add_u64 v[4:5], s[4:5], 0, v[4:5]
	v_lshl_add_u64 v[10:11], v[10:11], 0, s[6:7]
	v_lshl_add_u64 v[12:13], v[12:13], 0, s[6:7]
	v_lshl_add_u64 v[14:15], v[14:15], 0, s[6:7]
	v_lshl_add_u64 v[16:17], v[16:17], 0, s[6:7]
	v_lshl_add_u64 v[18:19], v[18:19], 0, s[6:7]
	v_lshl_add_u64 v[20:21], v[20:21], 0, v[66:67]
	v_lshl_add_u64 v[2:3], v[2:3], 0, v[66:67]
	v_lshl_add_u64 v[4:5], v[4:5], 0, s[6:7]
	v_lshl_add_u64 v[12:13], v[12:13], 0, v[66:67]
	v_lshl_add_u64 v[14:15], v[14:15], 0, v[66:67]
	v_lshl_add_u64 v[16:17], v[16:17], 0, v[66:67]
	v_lshl_add_u64 v[18:19], v[18:19], 0, v[66:67]
	global_load_dwordx4 v[58:61], v[20:21], off nt
	global_load_dwordx4 v[62:65], v[2:3], off nt
	global_load_dwordx4 v[50:53], v[16:17], off nt
	global_load_dwordx4 v[54:57], v[18:19], off nt
	global_load_dwordx4 v[38:41], v[12:13], off nt
	global_load_dwordx4 v[46:49], v[14:15], off nt
	v_lshl_add_u64 v[2:3], v[10:11], 0, v[66:67]
	v_lshl_add_u64 v[4:5], v[4:5], 0, v[66:67]
	global_load_dwordx4 v[42:45], v[2:3], off nt
	global_load_dwordx4 v[34:37], v[4:5], off nt
	s_cmp_eq_u32 s12, 1
	s_cselect_b32 s4, 5, 2
	s_and_b64 s[2:3], s[2:3], exec
	s_cselect_b32 s25, 4, s4
	s_add_u32 s16, s82, 0x13300000
	v_and_b32_e32 v68, 56, v8
	v_add_u32_e32 v2, s10, v66
	v_mul_u32_u24_e32 v3, 0x84, v70
	s_addc_u32 s17, s83, 0
	v_mul_u32_u24_e32 v4, 0x84, v68
	v_lshlrev_b32_e32 v5, 2, v70
	s_add_u32 s18, s82, 0x3300000
	v_add3_u32 v71, s10, v4, v5
	v_and_b32_e32 v72, 16, v5
	v_or_b32_e32 v75, 12, v5
	v_lshlrev_b32_e32 v66, 2, v6
	v_add_u32_e32 v76, v2, v3
	s_addc_u32 s19, s83, 0
	v_mov_b32_e32 v69, v67
	v_or_b32_e32 v73, 4, v72
	v_or_b32_e32 v74, 8, v72
	s_add_i32 s20, 0, 0x202b0
	s_add_i32 s21, 0, 0x202a8
	s_add_i32 s22, 0, 0x202a0
	s_mov_b32 s23, 0xc3e00000
	v_mov_b32_e32 v77, 0x43e00000
	s_mov_b32 s27, s11
	s_mov_b32 s26, s25
	s_mov_b64 s[4:5], s[0:1]
	s_waitcnt vmcnt(7)
	v_mov_b64_e32 v[6:7], v[58:59]
	s_waitcnt vmcnt(6)
	v_mov_b64_e32 v[2:3], v[62:63]
	s_waitcnt vmcnt(5)
	v_mov_b64_e32 v[14:15], v[50:51]
	s_waitcnt vmcnt(4)
	v_mov_b64_e32 v[10:11], v[54:55]
	s_waitcnt vmcnt(3)
	v_mov_b64_e32 v[22:23], v[38:39]
	s_waitcnt vmcnt(2)
	v_mov_b64_e32 v[18:19], v[46:47]
	v_mov_b64_e32 v[4:5], v[64:65]
	s_waitcnt vmcnt(1)
	v_mov_b64_e32 v[26:27], v[42:43]
	s_waitcnt vmcnt(0)
	v_mov_b64_e32 v[30:31], v[34:35]
	v_mov_b64_e32 v[8:9], v[60:61]
	v_mov_b64_e32 v[12:13], v[56:57]
	v_mov_b64_e32 v[16:17], v[52:53]
	v_mov_b64_e32 v[20:21], v[48:49]
	v_mov_b64_e32 v[24:25], v[40:41]
	v_mov_b64_e32 v[28:29], v[44:45]
	v_mov_b64_e32 v[32:33], v[36:37]
	s_branch .LBB0_77
.LBB0_76:
	s_waitcnt lgkmcnt(3)
	v_mul_f32_e32 v40, 0x43800000, v40
	v_mul_f32_e32 v41, 0x43800000, v41
	s_waitcnt lgkmcnt(2)
	v_mul_f32_e32 v43, 0x43800000, v38
	v_med3_f32 v40, v40, s23, v77
	v_med3_f32 v41, v41, s23, v77
	v_mov_b32_e32 v38, 0
	v_cvt_pk_fp8_f32 v38, v40, v41
	v_mul_f32_e32 v39, 0x43800000, v39
	v_med3_f32 v40, v43, s23, v77
	v_med3_f32 v39, v39, s23, v77
	s_waitcnt lgkmcnt(1)
	v_mul_f32_e32 v36, 0x43800000, v36
	v_mul_f32_e32 v37, 0x43800000, v37
	v_cvt_pk_fp8_f32 v38, v40, v39 op_sel:[0,0,1]
	v_med3_f32 v36, v36, s23, v77
	v_med3_f32 v37, v37, s23, v77
	v_mov_b32_e32 v39, 0
	v_cvt_pk_fp8_f32 v39, v36, v37
	s_waitcnt lgkmcnt(0)
	v_mul_f32_e32 v34, 0x43800000, v34
	v_mul_f32_e32 v35, 0x43800000, v35
	v_med3_f32 v34, v34, s23, v77
	v_med3_f32 v35, v35, s23, v77
	v_cvt_pk_fp8_f32 v39, v34, v35 op_sel:[0,0,1]
	v_or_b32_e32 v34, v42, v75
	v_ashrrev_i32_e32 v35, 31, v34
	v_lshlrev_b64 v[34:35], 10, v[34:35]
	v_lshl_add_u64 v[34:35], s[0:1], 0, v[34:35]
	v_lshl_add_u64 v[34:35], v[34:35], 0, s[6:7]
	v_lshl_add_u64 v[34:35], v[34:35], 0, v[68:69]
	global_store_dwordx2 v[34:35], v[38:39], off nt
	s_waitcnt lgkmcnt(0)
	s_waitcnt vmcnt(4)
	v_mov_b64_e32 v[36:37], v[32:33]
	v_mov_b64_e32 v[44:45], v[28:29]
	v_mov_b64_e32 v[40:41], v[24:25]
	v_mov_b64_e32 v[48:49], v[20:21]
	v_mov_b64_e32 v[52:53], v[16:17]
	v_mov_b64_e32 v[56:57], v[12:13]
	v_mov_b64_e32 v[60:61], v[8:9]
	v_mov_b64_e32 v[64:65], v[4:5]
	s_andn2_b64 vcc, exec, s[2:3]
	v_mov_b64_e32 v[34:35], v[30:31]
	v_mov_b64_e32 v[42:43], v[26:27]
	v_mov_b64_e32 v[38:39], v[22:23]
	v_mov_b64_e32 v[46:47], v[18:19]
	v_mov_b64_e32 v[50:51], v[14:15]
	v_mov_b64_e32 v[54:55], v[10:11]
	v_mov_b64_e32 v[58:59], v[6:7]
	v_mov_b64_e32 v[62:63], v[2:3]
	s_mov_b32 s11, s27
	s_mov_b32 s25, s26
	s_mov_b64 s[0:1], s[4:5]
	s_cbranch_vccz .LBB0_120

; #define GAS __attribute__((address_space(1)))
; #define LAS __attribute__((address_space(3)))
; __device__ __forceinline__ void titem_load(const TItem& T, int lane, f32x4 (&v)[8]) {
;     const int nblk = T.N / 32, kb = T.item / nblk, nb = T.item % nblk, k0 = 64 * kb, n0 = 32 * nb;
; #pragma unroll
;     for (int i = 0; i < 8; ++i) v[i] = *(const GAS f32x4*)(T.W + (size_t)(k0 + 8 * i + (lane >> 3)) * T.N + n0 + 4 * (lane & 7));
; }
; __device__ __forceinline__ TItem moe_item(Frame& F, int L, int r) {
;     constexpr int I_SQ = 16 * (1024 / 32);
;     const int mi = r / I_SQ, item = r % I_SQ, e = mi / 3, which = mi % 3;
;     const float* W = (which == 0 ? inp(F, I_WG) : which == 1 ? inp(F, I_WU) : inp(F, I_WD)) + (size_t)(L * 16 + e) * 1024 * 1024;
;     bf16_t* WT = (bf16_t*)(which < 2 ? F.ws + WS_WUP + (size_t)(L * 16 + e) * 2048 * 1024 : F.ws + WS_WDN + (size_t)(L * 16 + e) * 1024 * 1024);
;     return TItem{W, WT, 1024, which == 0 ? RM_UPG : which == 1 ? RM_UPU : RM_P8, item, true};
; }
; __device__ __forceinline__ void moe_convert_run(Frame& F, int L, int first, int end, int stride, LAS float* scr) {
;     if (first >= end) return;
;     f32x4 nv[8]; TItem nT = moe_item(F, L, first); titem_load(nT, F.lane, nv);
;     for (int r = first; r < end; r += stride) {
;         const TItem T = nT; f32x4 v[8];
; #pragma unroll
;         for (int i = 0; i < 8; ++i) v[i] = nv[i];
;         if (r + stride < end) { nT = moe_item(F, L, r + stride); titem_load(nT, F.lane, nv); }
.LBB0_86:
	s_mul_hi_i32 s4, s14, 0x2aaaaaab
	s_lshr_b32 s5, s4, 31
	s_ashr_i32 s4, s4, 8
	s_add_i32 s28, s4, s5
	s_ashr_i32 s29, s28, 31
	s_lshl_b64 s[4:5], s[28:29], 20
	s_lshl_b64 s[26:27], s[28:29], 21
	s_add_u32 s13, s18, s26
	s_addc_u32 s26, s19, s27
	s_add_u32 s4, s16, s4
	s_addc_u32 s5, s17, s5
	s_cmp_lt_i32 s9, 2
	s_cselect_b32 s5, s26, s5
	s_cselect_b32 s4, s13, s4
	s_cmp_eq_u32 s9, 1
	s_cselect_b32 s9, 5, 2
	s_and_b64 s[6:7], s[6:7], exec
	s_cselect_b32 s26, 4, s9
	s_lshl_b64 s[6:7], s[28:29], 22
	s_add_u32 s6, s10, s6
	s_addc_u32 s7, s12, s7
	s_lshl_b32 s8, s8, 9
	s_sub_i32 s27, s14, s8
	s_sext_i32_i16 s8, s27
	s_bfe_u32 s8, s8, 0x5001a
	s_add_i32 s8, s27, s8
	s_sext_i32_i16 s9, s8
	s_and_b32 s8, s8, 0xffe0
	s_lshl_b32 s9, s9, 1
	s_sub_i32 s8, s27, s8
	s_andn2_b32 s9, s9, 63
	s_sext_i32_i16 s8, s8
	v_or_b32_e32 v26, s9, v70
	s_lshl_b32 s8, s8, 5
	v_ashrrev_i32_e32 v27, 31, v26
	s_ashr_i32 s9, s8, 31
	v_lshlrev_b64 v[2:3], 12, v[26:27]
	v_lshl_add_u64 v[2:3], s[6:7], 0, v[2:3]
	s_lshl_b64 s[8:9], s[8:9], 2
	v_lshl_add_u64 v[2:3], v[2:3], 0, s[8:9]
	v_lshl_add_u64 v[10:11], v[2:3], 0, v[66:67]
	v_or_b32_e32 v2, 8, v26
	v_ashrrev_i32_e32 v3, 31, v2
	v_lshlrev_b64 v[2:3], 12, v[2:3]
	v_lshl_add_u64 v[2:3], s[6:7], 0, v[2:3]
	v_lshl_add_u64 v[2:3], v[2:3], 0, s[8:9]
	v_lshl_add_u64 v[12:13], v[2:3], 0, v[66:67]
	global_load_dwordx4 v[2:5], v[10:11], off nt
	global_load_dwordx4 v[6:9], v[12:13], off nt
	v_or_b32_e32 v10, 16, v26
	v_ashrrev_i32_e32 v11, 31, v10
	v_lshlrev_b64 v[10:11], 12, v[10:11]
	v_lshl_add_u64 v[10:11], s[6:7], 0, v[10:11]
	v_lshl_add_u64 v[10:11], v[10:11], 0, s[8:9]
	v_lshl_add_u64 v[18:19], v[10:11], 0, v[66:67]
	v_or_b32_e32 v10, 24, v26
	v_ashrrev_i32_e32 v11, 31, v10
	v_lshlrev_b64 v[10:11], 12, v[10:11]
	v_lshl_add_u64 v[10:11], s[6:7], 0, v[10:11]
	v_lshl_add_u64 v[10:11], v[10:11], 0, s[8:9]
	v_lshl_add_u64 v[20:21], v[10:11], 0, v[66:67]
	global_load_dwordx4 v[10:13], v[18:19], off nt
	global_load_dwordx4 v[14:17], v[20:21], off nt
	v_or_b32_e32 v18, 32, v26
	v_ashrrev_i32_e32 v19, 31, v18
	v_lshlrev_b64 v[18:19], 12, v[18:19]
	v_lshl_add_u64 v[18:19], s[6:7], 0, v[18:19]
	v_lshl_add_u64 v[18:19], v[18:19], 0, s[8:9]
	v_lshl_add_u64 v[28:29], v[18:19], 0, v[66:67]
	v_or_b32_e32 v18, 40, v26
	v_ashrrev_i32_e32 v19, 31, v18
	v_lshlrev_b64 v[18:19], 12, v[18:19]
	v_lshl_add_u64 v[18:19], s[6:7], 0, v[18:19]
	v_lshl_add_u64 v[18:19], v[18:19], 0, s[8:9]
	v_lshl_add_u64 v[30:31], v[18:19], 0, v[66:67]
	global_load_dwordx4 v[18:21], v[28:29], off nt
	global_load_dwordx4 v[22:25], v[30:31], off nt
	v_or_b32_e32 v28, 48, v26
	v_ashrrev_i32_e32 v29, 31, v28
	v_or_b32_e32 v26, 56, v26
	v_lshlrev_b64 v[28:29], 12, v[28:29]
	v_ashrrev_i32_e32 v27, 31, v26
	v_lshl_add_u64 v[28:29], s[6:7], 0, v[28:29]
	v_lshlrev_b64 v[26:27], 12, v[26:27]
	v_lshl_add_u64 v[28:29], v[28:29], 0, s[8:9]
	v_lshl_add_u64 v[26:27], s[6:7], 0, v[26:27]
	v_lshl_add_u64 v[78:79], v[28:29], 0, v[66:67]
	v_lshl_add_u64 v[26:27], v[26:27], 0, s[8:9]
	v_lshl_add_u64 v[80:81], v[26:27], 0, v[66:67]
	global_load_dwordx4 v[26:29], v[78:79], off nt
	global_load_dwordx4 v[30:33], v[80:81], off nt

; #define GAS __attribute__((address_space(1)))
; #define LAS __attribute__((address_space(3)))
; #define LDS_WAIT() asm volatile("s_waitcnt lgkmcnt(0)" ::: "memory")
; __device__ __forceinline__ unsigned pk2(float lo, float hi) { unsigned r; asm("v_cvt_pk_bf16_f32 %0, %1, %2" : "=v"(r) : "v"(lo), "v"(hi)); return r; }
; __device__ __forceinline__ void titem_store(const TItem& T, int lane, const f32x4 (&v)[8], LAS float* scr) {
;     const int nblk = T.N / 32, kb = T.item / nblk, nb = T.item % nblk, k0 = 64 * kb, n0 = 32 * nb;
; #pragma unroll
;     for (int i = 0; i < 8; ++i) { LAS float* s = scr + (8 * i + (lane >> 3)) * 33 + 4 * (lane & 7); s[0] = v[i][0]; s[1] = v[i][1]; s[2] = v[i][2]; s[3] = v[i][3]; }
;     LDS_WAIT(); asm volatile("" ::: "memory");
;     const int c = lane & 7;
; #pragma unroll
;     for (int j = 0; j < 4; ++j) { const int n = (lane >> 3) + 8 * j; const LAS float* s = scr + (8 * c) * 33 + n;
;         if (T.f8) { u32x2 o; o.x = pg8::pack4_fp8(s[0 * 33] * pg8::SC_W, s[1 * 33] * pg8::SC_W, s[2 * 33] * pg8::SC_W, s[3 * 33] * pg8::SC_W); o.y = pg8::pack4_fp8(s[4 * 33] * pg8::SC_W, s[5 * 33] * pg8::SC_W, s[6 * 33] * pg8::SC_W, s[7 * 33] * pg8::SC_W);
;             *(GAS u32x2*)((unsigned char*)T.WT + (size_t)row_map(T.mode, n0, n) * 1024 + k0 + 8 * c) = o; }
;         else { u32x4 o; o.x = pk2(s[0 * 33], s[1 * 33]); o.y = pk2(s[2 * 33], s[3 * 33]); o.z = pk2(s[4 * 33], s[5 * 33]); o.w = pk2(s[6 * 33], s[7 * 33]);
;             *(GAS u32x4*)(T.WT + (size_t)row_map(T.mode, n0, n) * 1024 + k0 + 8 * c) = o; } }
;     LDS_WAIT(); asm volatile("" ::: "memory");
; }
.LBB0_96:
	s_waitcnt lgkmcnt(3)
	v_mul_f32_e32 v40, 0x43800000, v40
	v_mul_f32_e32 v41, 0x43800000, v41
	s_waitcnt lgkmcnt(2)
	v_mul_f32_e32 v46, 0x43800000, v38
	v_med3_f32 v40, v40, s23, v77
	v_med3_f32 v41, v41, s23, v77
	v_mov_b32_e32 v38, v67
	v_cvt_pk_fp8_f32 v38, v40, v41
	v_mul_f32_e32 v39, 0x43800000, v39
	v_med3_f32 v40, v46, s23, v77
	v_med3_f32 v39, v39, s23, v77
	s_waitcnt lgkmcnt(1)
	v_mul_f32_e32 v36, 0x43800000, v36
	v_mul_f32_e32 v37, 0x43800000, v37
	v_cvt_pk_fp8_f32 v38, v40, v39 op_sel:[0,0,1]
	v_med3_f32 v36, v36, s23, v77
	v_med3_f32 v37, v37, s23, v77
	v_mov_b32_e32 v39, v67
	v_cvt_pk_fp8_f32 v39, v36, v37
	s_waitcnt lgkmcnt(0)
	v_mul_f32_e32 v34, 0x43800000, v34
	v_mul_f32_e32 v35, 0x43800000, v35
	v_med3_f32 v34, v34, s23, v77
	v_med3_f32 v35, v35, s23, v77
	v_cvt_pk_fp8_f32 v39, v34, v35 op_sel:[0,0,1]
	v_or_b32_e32 v34, v45, v72
	s_ashr_i32 s6, s10, 5
	v_ashrrev_i32_e32 v35, 31, v34
	s_lshl_b32 s6, s6, 6
	v_lshlrev_b64 v[34:35], 10, v[34:35]
	s_ashr_i32 s7, s6, 31
	v_lshl_add_u64 v[34:35], s[0:1], 0, v[34:35]
	v_lshl_add_u64 v[34:35], v[34:35], 0, s[6:7]
	v_lshl_add_u64 v[34:35], v[34:35], 0, v[68:69]
	global_store_dwordx2 v[34:35], v[38:39], off nt
	ds_read2_b32 v[40:41], v71 offset0:8 offset1:41
	ds_read2_b32 v[38:39], v71 offset0:74 offset1:107
	ds_read2_b32 v[36:37], v71 offset0:140 offset1:173
	ds_read2_b32 v[34:35], v71 offset0:206 offset1:239
	s_mov_b64 s[12:13], -1
	s_mov_b64 s[8:9], 0
	s_cmp_lt_i32 s25, 4
	s_mov_b64 s[10:11], 0
	s_cbranch_scc1 .LBB0_100
	s_cmp_lg_u32 s25, 4
	s_cselect_b64 s[10:11], -1, 0
	s_cbranch_execz .LBB0_101

; #define GAS __attribute__((address_space(1)))
; #define LAS __attribute__((address_space(3)))
; #define LDS_WAIT() asm volatile("s_waitcnt lgkmcnt(0)" ::: "memory")
; __device__ __forceinline__ unsigned pk2(float lo, float hi) { unsigned r; asm("v_cvt_pk_bf16_f32 %0, %1, %2" : "=v"(r) : "v"(lo), "v"(hi)); return r; }
; __device__ __forceinline__ void titem_store(const TItem& T, int lane, const f32x4 (&v)[8], LAS float* scr) {
;     const int nblk = T.N / 32, kb = T.item / nblk, nb = T.item % nblk, k0 = 64 * kb, n0 = 32 * nb;
; #pragma unroll
;     for (int i = 0; i < 8; ++i) { LAS float* s = scr + (8 * i + (lane >> 3)) * 33 + 4 * (lane & 7); s[0] = v[i][0]; s[1] = v[i][1]; s[2] = v[i][2]; s[3] = v[i][3]; }
;     LDS_WAIT(); asm volatile("" ::: "memory");
;     const int c = lane & 7;
; #pragma unroll
;     for (int j = 0; j < 4; ++j) { const int n = (lane >> 3) + 8 * j; const LAS float* s = scr + (8 * c) * 33 + n;
;         if (T.f8) { u32x2 o; o.x = pg8::pack4_fp8(s[0 * 33] * pg8::SC_W, s[1 * 33] * pg8::SC_W, s[2 * 33] * pg8::SC_W, s[3 * 33] * pg8::SC_W); o.y = pg8::pack4_fp8(s[4 * 33] * pg8::SC_W, s[5 * 33] * pg8::SC_W, s[6 * 33] * pg8::SC_W, s[7 * 33] * pg8::SC_W);
;             *(GAS u32x2*)((unsigned char*)T.WT + (size_t)row_map(T.mode, n0, n) * 1024 + k0 + 8 * c) = o; }
;         else { u32x4 o; o.x = pk2(s[0 * 33], s[1 * 33]); o.y = pk2(s[2 * 33], s[3 * 33]); o.z = pk2(s[4 * 33], s[5 * 33]); o.w = pk2(s[6 * 33], s[7 * 33]);
;             *(GAS u32x4*)(T.WT + (size_t)row_map(T.mode, n0, n) * 1024 + k0 + 8 * c) = o; } }
;     LDS_WAIT(); asm volatile("" ::: "memory");
; }
.LBB0_104:
	s_waitcnt lgkmcnt(3)
	v_mul_f32_e32 v40, 0x43800000, v40
	v_mul_f32_e32 v41, 0x43800000, v41
	s_waitcnt lgkmcnt(2)
	v_mul_f32_e32 v46, 0x43800000, v38
	v_med3_f32 v40, v40, s23, v77
	v_med3_f32 v41, v41, s23, v77
	v_mov_b32_e32 v38, v67
	v_cvt_pk_fp8_f32 v38, v40, v41
	v_mul_f32_e32 v39, 0x43800000, v39
	v_med3_f32 v40, v46, s23, v77
	v_med3_f32 v39, v39, s23, v77
	s_waitcnt lgkmcnt(1)
	v_mul_f32_e32 v36, 0x43800000, v36
	v_mul_f32_e32 v37, 0x43800000, v37
	v_cvt_pk_fp8_f32 v38, v40, v39 op_sel:[0,0,1]
	v_med3_f32 v36, v36, s23, v77
	v_med3_f32 v37, v37, s23, v77
	v_mov_b32_e32 v39, v67
	v_cvt_pk_fp8_f32 v39, v36, v37
	s_waitcnt lgkmcnt(0)
	v_mul_f32_e32 v34, 0x43800000, v34
	v_mul_f32_e32 v35, 0x43800000, v35
	v_med3_f32 v34, v34, s23, v77
	v_med3_f32 v35, v35, s23, v77
	v_cvt_pk_fp8_f32 v39, v34, v35 op_sel:[0,0,1]
	v_or_b32_e32 v34, v45, v73
	v_ashrrev_i32_e32 v35, 31, v34
	v_lshlrev_b64 v[34:35], 10, v[34:35]
	v_lshl_add_u64 v[34:35], s[0:1], 0, v[34:35]
	v_lshl_add_u64 v[34:35], v[34:35], 0, s[6:7]
	v_lshl_add_u64 v[34:35], v[34:35], 0, v[68:69]
	global_store_dwordx2 v[34:35], v[38:39], off nt
	ds_read2_b32 v[40:41], v71 offset0:16 offset1:49
	ds_read2_b32 v[38:39], v71 offset0:82 offset1:115
	ds_read2_b32 v[36:37], v71 offset0:148 offset1:181
	ds_read2_b32 v[34:35], v71 offset0:214 offset1:247
	s_mov_b64 s[12:13], -1
	s_mov_b64 s[8:9], 0
	s_cmp_lt_i32 s25, 4
	s_mov_b64 s[10:11], 0
	s_cbranch_scc1 .LBB0_108
	s_cmp_lg_u32 s25, 4
	s_cselect_b64 s[10:11], -1, 0
	s_cbranch_execz .LBB0_109

; #define GAS __attribute__((address_space(1)))
; #define LAS __attribute__((address_space(3)))
; #define LDS_WAIT() asm volatile("s_waitcnt lgkmcnt(0)" ::: "memory")
; __device__ __forceinline__ unsigned pk2(float lo, float hi) { unsigned r; asm("v_cvt_pk_bf16_f32 %0, %1, %2" : "=v"(r) : "v"(lo), "v"(hi)); return r; }
; __device__ __forceinline__ void titem_store(const TItem& T, int lane, const f32x4 (&v)[8], LAS float* scr) {
;     const int nblk = T.N / 32, kb = T.item / nblk, nb = T.item % nblk, k0 = 64 * kb, n0 = 32 * nb;
; #pragma unroll
;     for (int i = 0; i < 8; ++i) { LAS float* s = scr + (8 * i + (lane >> 3)) * 33 + 4 * (lane & 7); s[0] = v[i][0]; s[1] = v[i][1]; s[2] = v[i][2]; s[3] = v[i][3]; }
;     LDS_WAIT(); asm volatile("" ::: "memory");
;     const int c = lane & 7;
; #pragma unroll
;     for (int j = 0; j < 4; ++j) { const int n = (lane >> 3) + 8 * j; const LAS float* s = scr + (8 * c) * 33 + n;
;         if (T.f8) { u32x2 o; o.x = pg8::pack4_fp8(s[0 * 33] * pg8::SC_W, s[1 * 33] * pg8::SC_W, s[2 * 33] * pg8::SC_W, s[3 * 33] * pg8::SC_W); o.y = pg8::pack4_fp8(s[4 * 33] * pg8::SC_W, s[5 * 33] * pg8::SC_W, s[6 * 33] * pg8::SC_W, s[7 * 33] * pg8::SC_W);
;             *(GAS u32x2*)((unsigned char*)T.WT + (size_t)row_map(T.mode, n0, n) * 1024 + k0 + 8 * c) = o; }
;         else { u32x4 o; o.x = pk2(s[0 * 33], s[1 * 33]); o.y = pk2(s[2 * 33], s[3 * 33]); o.z = pk2(s[4 * 33], s[5 * 33]); o.w = pk2(s[6 * 33], s[7 * 33]);
;             *(GAS u32x4*)(T.WT + (size_t)row_map(T.mode, n0, n) * 1024 + k0 + 8 * c) = o; } }
;     LDS_WAIT(); asm volatile("" ::: "memory");
; }
.LBB0_112:
	s_waitcnt lgkmcnt(3)
	v_mul_f32_e32 v40, 0x43800000, v40
	v_mul_f32_e32 v41, 0x43800000, v41
	s_waitcnt lgkmcnt(2)
	v_mul_f32_e32 v46, 0x43800000, v38
	v_med3_f32 v40, v40, s23, v77
	v_med3_f32 v41, v41, s23, v77
	v_mov_b32_e32 v38, v67
	v_cvt_pk_fp8_f32 v38, v40, v41
	v_mul_f32_e32 v39, 0x43800000, v39
	v_med3_f32 v40, v46, s23, v77
	v_med3_f32 v39, v39, s23, v77
	s_waitcnt lgkmcnt(1)
	v_mul_f32_e32 v36, 0x43800000, v36
	v_mul_f32_e32 v37, 0x43800000, v37
	v_cvt_pk_fp8_f32 v38, v40, v39 op_sel:[0,0,1]
	v_med3_f32 v36, v36, s23, v77
	v_med3_f32 v37, v37, s23, v77
	v_mov_b32_e32 v39, v67
	v_cvt_pk_fp8_f32 v39, v36, v37
	s_waitcnt lgkmcnt(0)
	v_mul_f32_e32 v34, 0x43800000, v34
	v_mul_f32_e32 v35, 0x43800000, v35
	v_med3_f32 v34, v34, s23, v77
	v_med3_f32 v35, v35, s23, v77
	v_cvt_pk_fp8_f32 v39, v34, v35 op_sel:[0,0,1]
	v_or_b32_e32 v34, v45, v74
	v_ashrrev_i32_e32 v35, 31, v34
	v_lshlrev_b64 v[34:35], 10, v[34:35]
	v_lshl_add_u64 v[34:35], s[0:1], 0, v[34:35]
	v_lshl_add_u64 v[34:35], v[34:35], 0, s[6:7]
	v_lshl_add_u64 v[34:35], v[34:35], 0, v[68:69]
	global_store_dwordx2 v[34:35], v[38:39], off nt
	ds_read2_b32 v[40:41], v71 offset0:24 offset1:57
	ds_read2_b32 v[38:39], v71 offset0:90 offset1:123
	ds_read2_b32 v[36:37], v71 offset0:156 offset1:189
	ds_read2_b32 v[34:35], v71 offset0:222 offset1:255
	s_mov_b64 s[12:13], -1
	s_mov_b64 s[8:9], 0
	s_cmp_lt_i32 s25, 4
	s_mov_b64 s[10:11], 0
	s_cbranch_scc1 .LBB0_116
	s_cmp_lg_u32 s25, 4
	s_cselect_b64 s[10:11], -1, 0
	s_cbranch_execz .LBB0_117

; #define GAS __attribute__((address_space(1)))
; #define LAS __attribute__((address_space(3)))
; #define PHASE_FRAME(F0) Frame F = F0; { int t_ = threadIdx.x; asm volatile("" : "+v"(t_)); F.tid = t_; F.lane = t_ & 63; F.wave = __builtin_amdgcn_readfirstlane(t_ >> 6); }
; __device__ __forceinline__ void titem_load(const TItem& T, int lane, f32x4 (&v)[8]) {
;     const int nblk = T.N / 32, kb = T.item / nblk, nb = T.item % nblk, k0 = 64 * kb, n0 = 32 * nb;
; #pragma unroll
;     for (int i = 0; i < 8; ++i) v[i] = *(const GAS f32x4*)(T.W + (size_t)(k0 + 8 * i + (lane >> 3)) * T.N + n0 + 4 * (lane & 7));
; }
; __device__ __forceinline__ void moe_convert_run(Frame& F, int L, int first, int end, int stride, LAS float* scr) {
;     if (first >= end) return;
;     f32x4 nv[8]; TItem nT = moe_item(F, L, first); titem_load(nT, F.lane, nv);
;     for (int r = first; r < end; r += stride) {
;         const TItem T = nT; f32x4 v[8];
; #pragma unroll
;         for (int i = 0; i < 8; ++i) v[i] = nv[i];
;         if (r + stride < end) { nT = moe_item(F, L, r + stride); titem_load(nT, F.lane, nv); }
;         titem_store(T, F.lane, v, scr);
;     }
; }
; __device__ __forceinline__ void moe_convert_slice(const Frame& F0, int L, int first, int n, int rank, int n_idle) {
;     PHASE_FRAME(F0);
;     const int per = (n + n_idle - 1) / n_idle, lo = first + rank * per, hi = (lo + per < first + n) ? lo + per : first + n;
;     moe_convert_run(F, L, lo + F.wave, hi, 8, (LAS float*)(F.lds + F.wave * 16384));
.LBB0_492:
	s_mul_hi_i32 s0, s4, 0x2aaaaaab
	s_lshr_b32 s1, s0, 31
	s_ashr_i32 s0, s0, 8
	v_readlane_b32 s10, v255, 17
	s_add_i32 s0, s0, s1
	s_lshl_b32 s17, s10, 4
	v_readlane_b32 s11, v255, 18
	s_add_i32 s10, s0, s17
	s_lshl_b32 s1, s7, 14
	s_ashr_i32 s11, s10, 31
	s_add_i32 s22, s1, 0
	s_lshl_b64 s[0:1], s[10:11], 20
	s_lshl_b64 s[18:19], s[10:11], 21
	v_readlane_b32 s7, v253, 45
	s_add_u32 s7, s7, s18
	v_readlane_b32 s18, v253, 46
	s_addc_u32 s18, s18, s19
	v_readlane_b32 s19, v253, 43
	s_add_u32 s0, s19, s0
	v_readlane_b32 s19, v253, 44
	s_addc_u32 s1, s19, s1
	s_cmp_lt_i32 s5, 2
	s_cselect_b32 s1, s18, s1
	s_cselect_b32 s0, s7, s0
	s_lshl_b64 s[10:11], s[10:11], 22
	s_add_u32 s8, s8, s10
	s_addc_u32 s9, s9, s11
	s_lshl_b32 s6, s6, 9
	s_sub_i32 s10, s4, s6
	s_bfe_u32 s6, s10, 0x5001a
	s_add_i32 s6, s10, s6
	s_sext_i32_i16 s7, s6
	s_lshl_b32 s7, s7, 1
	v_bfe_u32 v1, v2, 3, 3
	s_andn2_b32 s7, s7, 63
	s_and_b32 s6, s6, 0xffe0
	v_or_b32_e32 v4, s7, v1
	s_sub_i32 s6, s10, s6
	s_sext_i32_i16 s6, s6
	v_or_b32_e32 v20, 8, v4
	s_lshl_b32 s6, s6, 5
	v_or_b32_e32 v10, 48, v4
	v_or_b32_e32 v12, 40, v4
	v_or_b32_e32 v14, 32, v4
	v_or_b32_e32 v16, 24, v4
	v_or_b32_e32 v18, 16, v4
	v_ashrrev_i32_e32 v21, 31, v20
	v_ashrrev_i32_e32 v5, 31, v4
	v_or_b32_e32 v6, 56, v4
	s_ashr_i32 s7, s6, 31
	v_lshlrev_b32_e32 v3, 2, v2
	v_ashrrev_i32_e32 v11, 31, v10
	v_ashrrev_i32_e32 v13, 31, v12
	v_ashrrev_i32_e32 v15, 31, v14
	v_ashrrev_i32_e32 v17, 31, v16
	v_ashrrev_i32_e32 v19, 31, v18
	v_lshlrev_b64 v[20:21], 12, v[20:21]
	v_lshlrev_b64 v[4:5], 12, v[4:5]
	v_ashrrev_i32_e32 v7, 31, v6
	s_lshl_b64 s[6:7], s[6:7], 2
	v_and_b32_e32 v8, 28, v3
	v_lshlrev_b64 v[10:11], 12, v[10:11]
	v_lshlrev_b64 v[12:13], 12, v[12:13]
	v_lshlrev_b64 v[14:15], 12, v[14:15]
	v_lshlrev_b64 v[16:17], 12, v[16:17]
	v_lshlrev_b64 v[18:19], 12, v[18:19]
	v_lshl_add_u64 v[20:21], s[8:9], 0, v[20:21]
	v_lshl_add_u64 v[4:5], s[8:9], 0, v[4:5]
	v_lshlrev_b64 v[6:7], 12, v[6:7]
	v_lshlrev_b32_e32 v190, 2, v8
	v_lshl_add_u64 v[10:11], s[8:9], 0, v[10:11]
	v_lshl_add_u64 v[12:13], s[8:9], 0, v[12:13]
	v_lshl_add_u64 v[14:15], s[8:9], 0, v[14:15]
	v_lshl_add_u64 v[16:17], s[8:9], 0, v[16:17]
	v_lshl_add_u64 v[18:19], s[8:9], 0, v[18:19]
	v_lshl_add_u64 v[20:21], v[20:21], 0, s[6:7]
	v_lshl_add_u64 v[4:5], v[4:5], 0, s[6:7]
	v_lshl_add_u64 v[6:7], s[8:9], 0, v[6:7]
	v_lshl_add_u64 v[10:11], v[10:11], 0, s[6:7]
	v_lshl_add_u64 v[12:13], v[12:13], 0, s[6:7]
	v_lshl_add_u64 v[14:15], v[14:15], 0, s[6:7]
	v_lshl_add_u64 v[16:17], v[16:17], 0, s[6:7]
	v_lshl_add_u64 v[18:19], v[18:19], 0, s[6:7]
	v_lshl_add_u64 v[20:21], v[20:21], 0, v[190:191]
	v_lshl_add_u64 v[4:5], v[4:5], 0, v[190:191]
	v_lshl_add_u64 v[6:7], v[6:7], 0, s[6:7]
	v_lshl_add_u64 v[12:13], v[12:13], 0, v[190:191]
	v_lshl_add_u64 v[14:15], v[14:15], 0, v[190:191]
	v_lshl_add_u64 v[16:17], v[16:17], 0, v[190:191]
	v_lshl_add_u64 v[18:19], v[18:19], 0, v[190:191]
	global_load_dwordx4 v[58:61], v[20:21], off nt
	global_load_dwordx4 v[62:65], v[4:5], off nt
	global_load_dwordx4 v[50:53], v[16:17], off nt
	global_load_dwordx4 v[54:57], v[18:19], off nt
	global_load_dwordx4 v[42:45], v[12:13], off nt
	global_load_dwordx4 v[46:49], v[14:15], off nt
	v_lshl_add_u64 v[4:5], v[10:11], 0, v[190:191]
	v_lshl_add_u64 v[6:7], v[6:7], 0, v[190:191]
	global_load_dwordx4 v[38:41], v[4:5], off nt
	global_load_dwordx4 v[34:37], v[6:7], off nt
	v_lshlrev_b32_e32 v5, 3, v2
	s_cmp_eq_u32 s5, 1
	v_and_b32_e32 v66, 56, v5
	s_cselect_b32 s5, 5, 2
	s_and_b64 s[2:3], s[2:3], exec
	v_add_u32_e32 v3, s22, v190
	v_mul_u32_u24_e32 v4, 0x84, v1
	v_mul_u32_u24_e32 v5, 0x84, v66
	v_bfe_u32 v68, v2, 3, 2
	v_lshlrev_b32_e32 v2, 2, v1
	s_cselect_b32 s23, 4, s5
	v_add3_u32 v69, s22, v5, v2
	v_and_b32_e32 v70, 16, v2
	v_or_b32_e32 v73, 12, v2
	v_lshlrev_b32_e32 v190, 2, v8
	v_add_u32_e32 v74, v3, v4
	v_mov_b32_e32 v67, v191
	v_or_b32_e32 v71, 4, v70
	v_or_b32_e32 v72, 8, v70
	s_add_i32 s22, s4, 8
	s_mov_b32 s28, s10
	s_mov_b32 s25, s23
	s_mov_b64 s[4:5], s[0:1]
	s_waitcnt vmcnt(0)
	v_mov_b64_e32 v[6:7], v[58:59]
	v_mov_b64_e32 v[2:3], v[62:63]
	v_mov_b64_e32 v[14:15], v[50:51]
	v_mov_b64_e32 v[10:11], v[54:55]
	v_mov_b64_e32 v[22:23], v[42:43]
	v_mov_b64_e32 v[18:19], v[46:47]
	v_mov_b64_e32 v[4:5], v[64:65]
	v_mov_b64_e32 v[26:27], v[38:39]
	v_mov_b64_e32 v[30:31], v[34:35]
	v_mov_b64_e32 v[8:9], v[60:61]
	v_mov_b64_e32 v[12:13], v[56:57]
	v_mov_b64_e32 v[16:17], v[52:53]
	v_mov_b64_e32 v[20:21], v[48:49]
	v_mov_b64_e32 v[24:25], v[44:45]
	v_mov_b64_e32 v[28:29], v[40:41]
	v_mov_b64_e32 v[32:33], v[36:37]
	s_branch .LBB0_494
.LBB0_493:
	s_waitcnt lgkmcnt(3)
	v_mul_f32_e32 v40, 0x43800000, v40
	v_mul_f32_e32 v41, 0x43800000, v41
	s_waitcnt lgkmcnt(2)
	v_mul_f32_e32 v43, 0x43800000, v38
	v_med3_f32 v40, v40, s15, v212
	v_med3_f32 v41, v41, s15, v212
	v_mov_b32_e32 v38, v191
	v_cvt_pk_fp8_f32 v38, v40, v41
	v_mul_f32_e32 v39, 0x43800000, v39
	v_med3_f32 v40, v43, s15, v212
	v_med3_f32 v39, v39, s15, v212
	s_waitcnt lgkmcnt(1)
	v_mul_f32_e32 v36, 0x43800000, v36
	v_mul_f32_e32 v37, 0x43800000, v37
	v_cvt_pk_fp8_f32 v38, v40, v39 op_sel:[0,0,1]
	v_med3_f32 v36, v36, s15, v212
	v_med3_f32 v37, v37, s15, v212
	v_mov_b32_e32 v39, v191
	v_cvt_pk_fp8_f32 v39, v36, v37
	s_waitcnt lgkmcnt(0)
	v_mul_f32_e32 v34, 0x43800000, v34
	v_mul_f32_e32 v35, 0x43800000, v35
	v_med3_f32 v34, v34, s15, v212
	v_med3_f32 v35, v35, s15, v212
	v_cvt_pk_fp8_f32 v39, v34, v35 op_sel:[0,0,1]
	v_or_b32_e32 v34, v42, v73
	v_ashrrev_i32_e32 v35, 31, v34
	v_lshlrev_b64 v[34:35], 10, v[34:35]
	v_lshl_add_u64 v[34:35], s[0:1], 0, v[34:35]
	v_lshl_add_u64 v[34:35], v[34:35], 0, s[6:7]
	v_lshl_add_u64 v[34:35], v[34:35], 0, v[66:67]
	global_store_dwordx2 v[34:35], v[38:39], off nt
	s_waitcnt lgkmcnt(0)
	s_waitcnt vmcnt(4)
	v_mov_b64_e32 v[36:37], v[32:33]
	v_mov_b64_e32 v[40:41], v[28:29]
	v_mov_b64_e32 v[44:45], v[24:25]
	v_mov_b64_e32 v[48:49], v[20:21]
	v_mov_b64_e32 v[52:53], v[16:17]
	v_mov_b64_e32 v[56:57], v[12:13]
	v_mov_b64_e32 v[60:61], v[8:9]
	v_mov_b64_e32 v[64:65], v[4:5]
	s_add_i32 s22, s22, 8
	s_andn2_b64 vcc, exec, s[2:3]
	v_mov_b64_e32 v[34:35], v[30:31]
	v_mov_b64_e32 v[38:39], v[26:27]
	v_mov_b64_e32 v[42:43], v[22:23]
	v_mov_b64_e32 v[46:47], v[18:19]
	v_mov_b64_e32 v[50:51], v[14:15]
	v_mov_b64_e32 v[54:55], v[10:11]
	v_mov_b64_e32 v[58:59], v[6:7]
	v_mov_b64_e32 v[62:63], v[2:3]
	s_mov_b32 s10, s28
	s_mov_b32 s23, s25
	s_mov_b64 s[0:1], s[4:5]
	s_cbranch_vccz .LBB0_537

; #define GAS __attribute__((address_space(1)))
; #define LAS __attribute__((address_space(3)))
; __device__ __forceinline__ void titem_load(const TItem& T, int lane, f32x4 (&v)[8]) {
;     const int nblk = T.N / 32, kb = T.item / nblk, nb = T.item % nblk, k0 = 64 * kb, n0 = 32 * nb;
; #pragma unroll
;     for (int i = 0; i < 8; ++i) v[i] = *(const GAS f32x4*)(T.W + (size_t)(k0 + 8 * i + (lane >> 3)) * T.N + n0 + 4 * (lane & 7));
; }
; __device__ __forceinline__ TItem moe_item(Frame& F, int L, int r) {
;     constexpr int I_SQ = 16 * (1024 / 32);
;     const int mi = r / I_SQ, item = r % I_SQ, e = mi / 3, which = mi % 3;
;     const float* W = (which == 0 ? inp(F, I_WG) : which == 1 ? inp(F, I_WU) : inp(F, I_WD)) + (size_t)(L * 16 + e) * 1024 * 1024;
;     bf16_t* WT = (bf16_t*)(which < 2 ? F.ws + WS_WUP + (size_t)(L * 16 + e) * 2048 * 1024 : F.ws + WS_WDN + (size_t)(L * 16 + e) * 1024 * 1024);
;     return TItem{W, WT, 1024, which == 0 ? RM_UPG : which == 1 ? RM_UPU : RM_P8, item, true};
; }
; __device__ __forceinline__ void moe_convert_run(Frame& F, int L, int first, int end, int stride, LAS float* scr) {
;     if (first >= end) return;
;     f32x4 nv[8]; TItem nT = moe_item(F, L, first); titem_load(nT, F.lane, nv);
;     for (int r = first; r < end; r += stride) {
;         const TItem T = nT; f32x4 v[8];
; #pragma unroll
;         for (int i = 0; i < 8; ++i) v[i] = nv[i];
;         if (r + stride < end) { nT = moe_item(F, L, r + stride); titem_load(nT, F.lane, nv); }
.LBB0_503:
	s_mul_hi_i32 s4, s22, 0x2aaaaaab
	s_lshr_b32 s5, s4, 31
	s_ashr_i32 s4, s4, 8
	s_add_i32 s4, s4, s5
	s_add_i32 s28, s4, s17
	s_ashr_i32 s29, s28, 31
	s_lshl_b64 s[4:5], s[28:29], 20
	s_lshl_b64 s[30:31], s[28:29], 21
	v_readlane_b32 s19, v253, 45
	s_add_u32 s19, s19, s30
	v_readlane_b32 s25, v253, 46
	s_addc_u32 s25, s25, s31
	v_readlane_b32 s30, v253, 43
	s_add_u32 s4, s30, s4
	v_readlane_b32 s30, v253, 44
	s_addc_u32 s5, s30, s5
	s_cmp_lt_i32 s9, 2
	s_cselect_b32 s5, s25, s5
	s_cselect_b32 s4, s19, s4
	s_cmp_eq_u32 s9, 1
	s_cselect_b32 s9, 5, 2
	s_and_b64 s[6:7], s[6:7], exec
	s_cselect_b32 s25, 4, s9
	s_lshl_b64 s[6:7], s[28:29], 22
	s_add_u32 s6, s11, s6
	s_addc_u32 s7, s18, s7
	s_lshl_b32 s8, s8, 9
	s_sub_i32 s28, s22, s8
	s_sext_i32_i16 s8, s28
	s_bfe_u32 s8, s8, 0x5001a
	s_add_i32 s8, s28, s8
	s_sext_i32_i16 s9, s8
	s_lshl_b32 s9, s9, 1
	s_andn2_b32 s9, s9, 63
	s_and_b32 s8, s8, 0xffe0
	v_or_b32_e32 v26, s9, v1
	s_sub_i32 s8, s28, s8
	v_ashrrev_i32_e32 v27, 31, v26
	s_sext_i32_i16 s8, s8
	v_lshlrev_b64 v[2:3], 12, v[26:27]
	v_or_b32_e32 v4, 8, v26
	v_or_b32_e32 v10, 16, v26
	v_or_b32_e32 v12, 24, v26
	v_or_b32_e32 v18, 32, v26
	v_or_b32_e32 v20, 40, v26
	v_or_b32_e32 v28, 48, v26
	v_or_b32_e32 v26, 56, v26
	s_lshl_b32 s8, s8, 5
	v_ashrrev_i32_e32 v5, 31, v4
	v_ashrrev_i32_e32 v11, 31, v10
	v_ashrrev_i32_e32 v13, 31, v12
	v_ashrrev_i32_e32 v19, 31, v18
	v_ashrrev_i32_e32 v21, 31, v20
	v_ashrrev_i32_e32 v29, 31, v28
	v_ashrrev_i32_e32 v27, 31, v26
	s_ashr_i32 s9, s8, 31
	v_lshlrev_b64 v[4:5], 12, v[4:5]
	v_lshlrev_b64 v[10:11], 12, v[10:11]
	v_lshlrev_b64 v[12:13], 12, v[12:13]
	v_lshlrev_b64 v[18:19], 12, v[18:19]
	v_lshlrev_b64 v[20:21], 12, v[20:21]
	v_lshlrev_b64 v[28:29], 12, v[28:29]
	v_lshlrev_b64 v[26:27], 12, v[26:27]
	v_lshl_add_u64 v[2:3], s[6:7], 0, v[2:3]
	s_lshl_b64 s[8:9], s[8:9], 2
	v_lshl_add_u64 v[4:5], s[6:7], 0, v[4:5]
	v_lshl_add_u64 v[10:11], s[6:7], 0, v[10:11]
	v_lshl_add_u64 v[12:13], s[6:7], 0, v[12:13]
	v_lshl_add_u64 v[18:19], s[6:7], 0, v[18:19]
	v_lshl_add_u64 v[20:21], s[6:7], 0, v[20:21]
	v_lshl_add_u64 v[28:29], s[6:7], 0, v[28:29]
	v_lshl_add_u64 v[26:27], s[6:7], 0, v[26:27]
	v_lshl_add_u64 v[2:3], v[2:3], 0, s[8:9]
	v_lshl_add_u64 v[4:5], v[4:5], 0, s[8:9]
	v_lshl_add_u64 v[10:11], v[10:11], 0, s[8:9]
	v_lshl_add_u64 v[12:13], v[12:13], 0, s[8:9]
	v_lshl_add_u64 v[18:19], v[18:19], 0, s[8:9]
	v_lshl_add_u64 v[20:21], v[20:21], 0, s[8:9]
	v_lshl_add_u64 v[28:29], v[28:29], 0, s[8:9]
	v_lshl_add_u64 v[26:27], v[26:27], 0, s[8:9]
	v_lshl_add_u64 v[2:3], v[2:3], 0, v[190:191]
	v_lshl_add_u64 v[6:7], v[4:5], 0, v[190:191]
	v_lshl_add_u64 v[10:11], v[10:11], 0, v[190:191]
	v_lshl_add_u64 v[14:15], v[12:13], 0, v[190:191]
	v_lshl_add_u64 v[18:19], v[18:19], 0, v[190:191]
	v_lshl_add_u64 v[22:23], v[20:21], 0, v[190:191]
	v_lshl_add_u64 v[28:29], v[28:29], 0, v[190:191]
	v_lshl_add_u64 v[30:31], v[26:27], 0, v[190:191]
	global_load_dwordx4 v[2:5], v[2:3], off nt
	s_nop 0
	global_load_dwordx4 v[6:9], v[6:7], off nt
	s_nop 0
	global_load_dwordx4 v[10:13], v[10:11], off nt
	s_nop 0
	global_load_dwordx4 v[14:17], v[14:15], off nt
	s_nop 0
	global_load_dwordx4 v[18:21], v[18:19], off nt
	s_nop 0
	global_load_dwordx4 v[22:25], v[22:23], off nt
	s_nop 0
	global_load_dwordx4 v[26:29], v[28:29], off nt
	s_nop 0
	global_load_dwordx4 v[30:33], v[30:31], off nt

; #define GAS __attribute__((address_space(1)))
; #define LAS __attribute__((address_space(3)))
; #define LDS_WAIT() asm volatile("s_waitcnt lgkmcnt(0)" ::: "memory")
; __device__ __forceinline__ unsigned pk2(float lo, float hi) { unsigned r; asm("v_cvt_pk_bf16_f32 %0, %1, %2" : "=v"(r) : "v"(lo), "v"(hi)); return r; }
; __device__ __forceinline__ void titem_store(const TItem& T, int lane, const f32x4 (&v)[8], LAS float* scr) {
;     const int nblk = T.N / 32, kb = T.item / nblk, nb = T.item % nblk, k0 = 64 * kb, n0 = 32 * nb;
; #pragma unroll
;     for (int i = 0; i < 8; ++i) { LAS float* s = scr + (8 * i + (lane >> 3)) * 33 + 4 * (lane & 7); s[0] = v[i][0]; s[1] = v[i][1]; s[2] = v[i][2]; s[3] = v[i][3]; }
;     LDS_WAIT(); asm volatile("" ::: "memory");
;     const int c = lane & 7;
; #pragma unroll
;     for (int j = 0; j < 4; ++j) { const int n = (lane >> 3) + 8 * j; const LAS float* s = scr + (8 * c) * 33 + n;
;         if (T.f8) { u32x2 o; o.x = pg8::pack4_fp8(s[0 * 33] * pg8::SC_W, s[1 * 33] * pg8::SC_W, s[2 * 33] * pg8::SC_W, s[3 * 33] * pg8::SC_W); o.y = pg8::pack4_fp8(s[4 * 33] * pg8::SC_W, s[5 * 33] * pg8::SC_W, s[6 * 33] * pg8::SC_W, s[7 * 33] * pg8::SC_W);
;             *(GAS u32x2*)((unsigned char*)T.WT + (size_t)row_map(T.mode, n0, n) * 1024 + k0 + 8 * c) = o; }
;         else { u32x4 o; o.x = pk2(s[0 * 33], s[1 * 33]); o.y = pk2(s[2 * 33], s[3 * 33]); o.z = pk2(s[4 * 33], s[5 * 33]); o.w = pk2(s[6 * 33], s[7 * 33]);
;             *(GAS u32x4*)(T.WT + (size_t)row_map(T.mode, n0, n) * 1024 + k0 + 8 * c) = o; } }
;     LDS_WAIT(); asm volatile("" ::: "memory");
; }
.LBB0_513:
	s_waitcnt lgkmcnt(3)
	v_mul_f32_e32 v40, 0x43800000, v40
	v_mul_f32_e32 v41, 0x43800000, v41
	s_waitcnt lgkmcnt(2)
	v_mul_f32_e32 v46, 0x43800000, v38
	v_med3_f32 v40, v40, s15, v212
	v_med3_f32 v41, v41, s15, v212
	v_mov_b32_e32 v38, v191
	v_cvt_pk_fp8_f32 v38, v40, v41
	v_mul_f32_e32 v39, 0x43800000, v39
	v_med3_f32 v40, v46, s15, v212
	v_med3_f32 v39, v39, s15, v212
	s_waitcnt lgkmcnt(1)
	v_mul_f32_e32 v36, 0x43800000, v36
	v_mul_f32_e32 v37, 0x43800000, v37
	v_cvt_pk_fp8_f32 v38, v40, v39 op_sel:[0,0,1]
	v_med3_f32 v36, v36, s15, v212
	v_med3_f32 v37, v37, s15, v212
	v_mov_b32_e32 v39, v191
	v_cvt_pk_fp8_f32 v39, v36, v37
	s_waitcnt lgkmcnt(0)
	v_mul_f32_e32 v34, 0x43800000, v34
	v_mul_f32_e32 v35, 0x43800000, v35
	v_med3_f32 v34, v34, s15, v212
	v_med3_f32 v35, v35, s15, v212
	v_cvt_pk_fp8_f32 v39, v34, v35 op_sel:[0,0,1]
	v_or_b32_e32 v34, v45, v70
	s_ashr_i32 s6, s11, 5
	v_ashrrev_i32_e32 v35, 31, v34
	s_lshl_b32 s6, s6, 6
	v_lshlrev_b64 v[34:35], 10, v[34:35]
	s_ashr_i32 s7, s6, 31
	v_lshl_add_u64 v[34:35], s[0:1], 0, v[34:35]
	v_lshl_add_u64 v[34:35], v[34:35], 0, s[6:7]
	v_lshl_add_u64 v[34:35], v[34:35], 0, v[66:67]
	global_store_dwordx2 v[34:35], v[38:39], off nt
	ds_read2_b32 v[40:41], v69 offset0:8 offset1:41
	ds_read2_b32 v[38:39], v69 offset0:74 offset1:107
	ds_read2_b32 v[36:37], v69 offset0:140 offset1:173
	ds_read2_b32 v[34:35], v69 offset0:206 offset1:239
	s_mov_b64 s[18:19], -1
	s_mov_b64 s[8:9], 0
	s_cmp_lt_i32 s23, 4
	s_mov_b64 s[10:11], 0
	s_cbranch_scc1 .LBB0_517
	s_cmp_lg_u32 s23, 4
	s_cselect_b64 s[10:11], -1, 0
	s_cbranch_execz .LBB0_518

; #define GAS __attribute__((address_space(1)))
; #define LAS __attribute__((address_space(3)))
; #define LDS_WAIT() asm volatile("s_waitcnt lgkmcnt(0)" ::: "memory")
; __device__ __forceinline__ unsigned pk2(float lo, float hi) { unsigned r; asm("v_cvt_pk_bf16_f32 %0, %1, %2" : "=v"(r) : "v"(lo), "v"(hi)); return r; }
; __device__ __forceinline__ void titem_store(const TItem& T, int lane, const f32x4 (&v)[8], LAS float* scr) {
;     const int nblk = T.N / 32, kb = T.item / nblk, nb = T.item % nblk, k0 = 64 * kb, n0 = 32 * nb;
; #pragma unroll
;     for (int i = 0; i < 8; ++i) { LAS float* s = scr + (8 * i + (lane >> 3)) * 33 + 4 * (lane & 7); s[0] = v[i][0]; s[1] = v[i][1]; s[2] = v[i][2]; s[3] = v[i][3]; }
;     LDS_WAIT(); asm volatile("" ::: "memory");
;     const int c = lane & 7;
; #pragma unroll
;     for (int j = 0; j < 4; ++j) { const int n = (lane >> 3) + 8 * j; const LAS float* s = scr + (8 * c) * 33 + n;
;         if (T.f8) { u32x2 o; o.x = pg8::pack4_fp8(s[0 * 33] * pg8::SC_W, s[1 * 33] * pg8::SC_W, s[2 * 33] * pg8::SC_W, s[3 * 33] * pg8::SC_W); o.y = pg8::pack4_fp8(s[4 * 33] * pg8::SC_W, s[5 * 33] * pg8::SC_W, s[6 * 33] * pg8::SC_W, s[7 * 33] * pg8::SC_W);
;             *(GAS u32x2*)((unsigned char*)T.WT + (size_t)row_map(T.mode, n0, n) * 1024 + k0 + 8 * c) = o; }
;         else { u32x4 o; o.x = pk2(s[0 * 33], s[1 * 33]); o.y = pk2(s[2 * 33], s[3 * 33]); o.z = pk2(s[4 * 33], s[5 * 33]); o.w = pk2(s[6 * 33], s[7 * 33]);
;             *(GAS u32x4*)(T.WT + (size_t)row_map(T.mode, n0, n) * 1024 + k0 + 8 * c) = o; } }
;     LDS_WAIT(); asm volatile("" ::: "memory");
; }
.LBB0_521:
	s_waitcnt lgkmcnt(3)
	v_mul_f32_e32 v40, 0x43800000, v40
	v_mul_f32_e32 v41, 0x43800000, v41
	s_waitcnt lgkmcnt(2)
	v_mul_f32_e32 v46, 0x43800000, v38
	v_med3_f32 v40, v40, s15, v212
	v_med3_f32 v41, v41, s15, v212
	v_mov_b32_e32 v38, v191
	v_cvt_pk_fp8_f32 v38, v40, v41
	v_mul_f32_e32 v39, 0x43800000, v39
	v_med3_f32 v40, v46, s15, v212
	v_med3_f32 v39, v39, s15, v212
	s_waitcnt lgkmcnt(1)
	v_mul_f32_e32 v36, 0x43800000, v36
	v_mul_f32_e32 v37, 0x43800000, v37
	v_cvt_pk_fp8_f32 v38, v40, v39 op_sel:[0,0,1]
	v_med3_f32 v36, v36, s15, v212
	v_med3_f32 v37, v37, s15, v212
	v_mov_b32_e32 v39, v191
	v_cvt_pk_fp8_f32 v39, v36, v37
	s_waitcnt lgkmcnt(0)
	v_mul_f32_e32 v34, 0x43800000, v34
	v_mul_f32_e32 v35, 0x43800000, v35
	v_med3_f32 v34, v34, s15, v212
	v_med3_f32 v35, v35, s15, v212
	v_cvt_pk_fp8_f32 v39, v34, v35 op_sel:[0,0,1]
	v_or_b32_e32 v34, v45, v71
	v_ashrrev_i32_e32 v35, 31, v34
	v_lshlrev_b64 v[34:35], 10, v[34:35]
	v_lshl_add_u64 v[34:35], s[0:1], 0, v[34:35]
	v_lshl_add_u64 v[34:35], v[34:35], 0, s[6:7]
	v_lshl_add_u64 v[34:35], v[34:35], 0, v[66:67]
	global_store_dwordx2 v[34:35], v[38:39], off nt
	ds_read2_b32 v[40:41], v69 offset0:16 offset1:49
	ds_read2_b32 v[38:39], v69 offset0:82 offset1:115
	ds_read2_b32 v[36:37], v69 offset0:148 offset1:181
	ds_read2_b32 v[34:35], v69 offset0:214 offset1:247
	s_mov_b64 s[18:19], -1
	s_mov_b64 s[8:9], 0
	s_cmp_lt_i32 s23, 4
	s_mov_b64 s[10:11], 0
	s_cbranch_scc1 .LBB0_525
	s_cmp_lg_u32 s23, 4
	s_cselect_b64 s[10:11], -1, 0
	s_cbranch_execz .LBB0_526

; #define GAS __attribute__((address_space(1)))
; #define LAS __attribute__((address_space(3)))
; #define LDS_WAIT() asm volatile("s_waitcnt lgkmcnt(0)" ::: "memory")
; __device__ __forceinline__ unsigned pk2(float lo, float hi) { unsigned r; asm("v_cvt_pk_bf16_f32 %0, %1, %2" : "=v"(r) : "v"(lo), "v"(hi)); return r; }
; __device__ __forceinline__ void titem_store(const TItem& T, int lane, const f32x4 (&v)[8], LAS float* scr) {
;     const int nblk = T.N / 32, kb = T.item / nblk, nb = T.item % nblk, k0 = 64 * kb, n0 = 32 * nb;
; #pragma unroll
;     for (int i = 0; i < 8; ++i) { LAS float* s = scr + (8 * i + (lane >> 3)) * 33 + 4 * (lane & 7); s[0] = v[i][0]; s[1] = v[i][1]; s[2] = v[i][2]; s[3] = v[i][3]; }
;     LDS_WAIT(); asm volatile("" ::: "memory");
;     const int c = lane & 7;
; #pragma unroll
;     for (int j = 0; j < 4; ++j) { const int n = (lane >> 3) + 8 * j; const LAS float* s = scr + (8 * c) * 33 + n;
;         if (T.f8) { u32x2 o; o.x = pg8::pack4_fp8(s[0 * 33] * pg8::SC_W, s[1 * 33] * pg8::SC_W, s[2 * 33] * pg8::SC_W, s[3 * 33] * pg8::SC_W); o.y = pg8::pack4_fp8(s[4 * 33] * pg8::SC_W, s[5 * 33] * pg8::SC_W, s[6 * 33] * pg8::SC_W, s[7 * 33] * pg8::SC_W);
;             *(GAS u32x2*)((unsigned char*)T.WT + (size_t)row_map(T.mode, n0, n) * 1024 + k0 + 8 * c) = o; }
;         else { u32x4 o; o.x = pk2(s[0 * 33], s[1 * 33]); o.y = pk2(s[2 * 33], s[3 * 33]); o.z = pk2(s[4 * 33], s[5 * 33]); o.w = pk2(s[6 * 33], s[7 * 33]);
;             *(GAS u32x4*)(T.WT + (size_t)row_map(T.mode, n0, n) * 1024 + k0 + 8 * c) = o; } }
;     LDS_WAIT(); asm volatile("" ::: "memory");
; }
.LBB0_529:
	s_waitcnt lgkmcnt(3)
	v_mul_f32_e32 v40, 0x43800000, v40
	v_mul_f32_e32 v41, 0x43800000, v41
	s_waitcnt lgkmcnt(2)
	v_mul_f32_e32 v46, 0x43800000, v38
	v_med3_f32 v40, v40, s15, v212
	v_med3_f32 v41, v41, s15, v212
	v_mov_b32_e32 v38, v191
	v_cvt_pk_fp8_f32 v38, v40, v41
	v_mul_f32_e32 v39, 0x43800000, v39
	v_med3_f32 v40, v46, s15, v212
	v_med3_f32 v39, v39, s15, v212
	s_waitcnt lgkmcnt(1)
	v_mul_f32_e32 v36, 0x43800000, v36
	v_mul_f32_e32 v37, 0x43800000, v37
	v_cvt_pk_fp8_f32 v38, v40, v39 op_sel:[0,0,1]
	v_med3_f32 v36, v36, s15, v212
	v_med3_f32 v37, v37, s15, v212
	v_mov_b32_e32 v39, v191
	v_cvt_pk_fp8_f32 v39, v36, v37
	s_waitcnt lgkmcnt(0)
	v_mul_f32_e32 v34, 0x43800000, v34
	v_mul_f32_e32 v35, 0x43800000, v35
	v_med3_f32 v34, v34, s15, v212
	v_med3_f32 v35, v35, s15, v212
	v_cvt_pk_fp8_f32 v39, v34, v35 op_sel:[0,0,1]
	v_or_b32_e32 v34, v45, v72
	v_ashrrev_i32_e32 v35, 31, v34
	v_lshlrev_b64 v[34:35], 10, v[34:35]
	v_lshl_add_u64 v[34:35], s[0:1], 0, v[34:35]
	v_lshl_add_u64 v[34:35], v[34:35], 0, s[6:7]
	v_lshl_add_u64 v[34:35], v[34:35], 0, v[66:67]
	global_store_dwordx2 v[34:35], v[38:39], off nt
	ds_read2_b32 v[40:41], v69 offset0:24 offset1:57
	ds_read2_b32 v[38:39], v69 offset0:90 offset1:123
	ds_read2_b32 v[36:37], v69 offset0:156 offset1:189
	ds_read2_b32 v[34:35], v69 offset0:222 offset1:255
	s_mov_b64 s[18:19], -1
	s_mov_b64 s[8:9], 0
	s_cmp_lt_i32 s23, 4
	s_mov_b64 s[10:11], 0
	s_cbranch_scc1 .LBB0_533
	s_cmp_lg_u32 s23, 4
	s_cselect_b64 s[10:11], -1, 0
	s_cbranch_execz .LBB0_534

; #define GAS __attribute__((address_space(1)))
; #define LAS __attribute__((address_space(3)))
; #define PHASE_FRAME(F0) Frame F = F0; { int t_ = threadIdx.x; asm volatile("" : "+v"(t_)); F.tid = t_; F.lane = t_ & 63; F.wave = __builtin_amdgcn_readfirstlane(t_ >> 6); }
; __device__ __forceinline__ void titem_load(const TItem& T, int lane, f32x4 (&v)[8]) {
;     const int nblk = T.N / 32, kb = T.item / nblk, nb = T.item % nblk, k0 = 64 * kb, n0 = 32 * nb;
; #pragma unroll
;     for (int i = 0; i < 8; ++i) v[i] = *(const GAS f32x4*)(T.W + (size_t)(k0 + 8 * i + (lane >> 3)) * T.N + n0 + 4 * (lane & 7));
; }
; __device__ __forceinline__ void moe_convert_run(Frame& F, int L, int first, int end, int stride, LAS float* scr) {
;     if (first >= end) return;
;     f32x4 nv[8]; TItem nT = moe_item(F, L, first); titem_load(nT, F.lane, nv);
;     for (int r = first; r < end; r += stride) {
;         const TItem T = nT; f32x4 v[8];
; #pragma unroll
;         for (int i = 0; i < 8; ++i) v[i] = nv[i];
;         if (r + stride < end) { nT = moe_item(F, L, r + stride); titem_load(nT, F.lane, nv); }
;         titem_store(T, F.lane, v, scr);
;     }
; }
; __device__ __forceinline__ void moe_convert_slice(const Frame& F0, int L, int first, int n, int rank, int n_idle) {
;     PHASE_FRAME(F0);
;     const int per = (n + n_idle - 1) / n_idle, lo = first + rank * per, hi = (lo + per < first + n) ? lo + per : first + n;
;     moe_convert_run(F, L, lo + F.wave, hi, 8, (LAS float*)(F.lds + F.wave * 16384));
.LBB0_791:
	s_mul_hi_i32 s0, s4, 0x2aaaaaab
	s_lshr_b32 s1, s0, 31
	s_ashr_i32 s0, s0, 8
	v_readlane_b32 s10, v255, 17
	s_add_i32 s0, s0, s1
	s_lshl_b32 s17, s10, 4
	v_readlane_b32 s11, v255, 18
	s_add_i32 s10, s0, s17
	s_lshl_b32 s1, s7, 14
	s_ashr_i32 s11, s10, 31
	s_add_i32 s22, s1, 0
	s_lshl_b64 s[0:1], s[10:11], 20
	s_lshl_b64 s[18:19], s[10:11], 21
	v_readlane_b32 s7, v253, 45
	s_add_u32 s7, s7, s18
	v_readlane_b32 s18, v253, 46
	s_addc_u32 s18, s18, s19
	v_readlane_b32 s19, v253, 43
	s_add_u32 s0, s19, s0
	v_readlane_b32 s19, v253, 44
	s_addc_u32 s1, s19, s1
	s_cmp_lt_i32 s5, 2
	s_cselect_b32 s1, s18, s1
	s_cselect_b32 s0, s7, s0
	s_lshl_b64 s[10:11], s[10:11], 22
	s_add_u32 s8, s8, s10
	s_addc_u32 s9, s9, s11
	s_lshl_b32 s6, s6, 9
	s_sub_i32 s10, s4, s6
	s_bfe_u32 s6, s10, 0x5001a
	s_add_i32 s6, s10, s6
	s_sext_i32_i16 s7, s6
	s_lshl_b32 s7, s7, 1
	v_bfe_u32 v1, v2, 3, 3
	s_andn2_b32 s7, s7, 63
	s_and_b32 s6, s6, 0xffe0
	v_or_b32_e32 v4, s7, v1
	s_sub_i32 s6, s10, s6
	s_sext_i32_i16 s6, s6
	v_or_b32_e32 v20, 8, v4
	s_lshl_b32 s6, s6, 5
	v_or_b32_e32 v10, 48, v4
	v_or_b32_e32 v12, 40, v4
	v_or_b32_e32 v14, 32, v4
	v_or_b32_e32 v16, 24, v4
	v_or_b32_e32 v18, 16, v4
	v_ashrrev_i32_e32 v21, 31, v20
	v_ashrrev_i32_e32 v5, 31, v4
	v_or_b32_e32 v6, 56, v4
	s_ashr_i32 s7, s6, 31
	v_lshlrev_b32_e32 v3, 2, v2
	v_ashrrev_i32_e32 v11, 31, v10
	v_ashrrev_i32_e32 v13, 31, v12
	v_ashrrev_i32_e32 v15, 31, v14
	v_ashrrev_i32_e32 v17, 31, v16
	v_ashrrev_i32_e32 v19, 31, v18
	v_lshlrev_b64 v[20:21], 12, v[20:21]
	v_lshlrev_b64 v[4:5], 12, v[4:5]
	v_ashrrev_i32_e32 v7, 31, v6
	s_lshl_b64 s[6:7], s[6:7], 2
	v_and_b32_e32 v8, 28, v3
	v_lshlrev_b64 v[10:11], 12, v[10:11]
	v_lshlrev_b64 v[12:13], 12, v[12:13]
	v_lshlrev_b64 v[14:15], 12, v[14:15]
	v_lshlrev_b64 v[16:17], 12, v[16:17]
	v_lshlrev_b64 v[18:19], 12, v[18:19]
	v_lshl_add_u64 v[20:21], s[8:9], 0, v[20:21]
	v_lshl_add_u64 v[4:5], s[8:9], 0, v[4:5]
	v_lshlrev_b64 v[6:7], 12, v[6:7]
	v_lshlrev_b32_e32 v190, 2, v8
	v_lshl_add_u64 v[10:11], s[8:9], 0, v[10:11]
	v_lshl_add_u64 v[12:13], s[8:9], 0, v[12:13]
	v_lshl_add_u64 v[14:15], s[8:9], 0, v[14:15]
	v_lshl_add_u64 v[16:17], s[8:9], 0, v[16:17]
	v_lshl_add_u64 v[18:19], s[8:9], 0, v[18:19]
	v_lshl_add_u64 v[20:21], v[20:21], 0, s[6:7]
	v_lshl_add_u64 v[4:5], v[4:5], 0, s[6:7]
	v_lshl_add_u64 v[6:7], s[8:9], 0, v[6:7]
	v_lshl_add_u64 v[10:11], v[10:11], 0, s[6:7]
	v_lshl_add_u64 v[12:13], v[12:13], 0, s[6:7]
	v_lshl_add_u64 v[14:15], v[14:15], 0, s[6:7]
	v_lshl_add_u64 v[16:17], v[16:17], 0, s[6:7]
	v_lshl_add_u64 v[18:19], v[18:19], 0, s[6:7]
	v_lshl_add_u64 v[20:21], v[20:21], 0, v[190:191]
	v_lshl_add_u64 v[4:5], v[4:5], 0, v[190:191]
	v_lshl_add_u64 v[6:7], v[6:7], 0, s[6:7]
	v_lshl_add_u64 v[12:13], v[12:13], 0, v[190:191]
	v_lshl_add_u64 v[14:15], v[14:15], 0, v[190:191]
	v_lshl_add_u64 v[16:17], v[16:17], 0, v[190:191]
	v_lshl_add_u64 v[18:19], v[18:19], 0, v[190:191]
	global_load_dwordx4 v[58:61], v[20:21], off nt
	global_load_dwordx4 v[62:65], v[4:5], off nt
	global_load_dwordx4 v[50:53], v[16:17], off nt
	global_load_dwordx4 v[54:57], v[18:19], off nt
	global_load_dwordx4 v[42:45], v[12:13], off nt
	global_load_dwordx4 v[46:49], v[14:15], off nt
	v_lshl_add_u64 v[4:5], v[10:11], 0, v[190:191]
	v_lshl_add_u64 v[6:7], v[6:7], 0, v[190:191]
	global_load_dwordx4 v[38:41], v[4:5], off nt
	global_load_dwordx4 v[34:37], v[6:7], off nt
	v_lshlrev_b32_e32 v5, 3, v2
	s_cmp_eq_u32 s5, 1
	v_and_b32_e32 v66, 56, v5
	s_cselect_b32 s5, 5, 2
	s_and_b64 s[2:3], s[2:3], exec
	v_add_u32_e32 v3, s22, v190
	v_mul_u32_u24_e32 v4, 0x84, v1
	v_mul_u32_u24_e32 v5, 0x84, v66
	v_bfe_u32 v68, v2, 3, 2
	v_lshlrev_b32_e32 v2, 2, v1
	s_cselect_b32 s23, 4, s5
	v_add3_u32 v69, s22, v5, v2
	v_and_b32_e32 v70, 16, v2
	v_or_b32_e32 v73, 12, v2
	v_lshlrev_b32_e32 v190, 2, v8
	v_add_u32_e32 v74, v3, v4
	v_mov_b32_e32 v67, v191
	v_or_b32_e32 v71, 4, v70
	v_or_b32_e32 v72, 8, v70
	s_add_i32 s22, s4, 8
	s_mov_b32 s28, s10
	s_mov_b32 s25, s23
	s_mov_b64 s[4:5], s[0:1]
	s_waitcnt vmcnt(7)
	v_mov_b64_e32 v[6:7], v[58:59]
	s_waitcnt vmcnt(6)
	v_mov_b64_e32 v[2:3], v[62:63]
	s_waitcnt vmcnt(5)
	v_mov_b64_e32 v[14:15], v[50:51]
	s_waitcnt vmcnt(4)
	v_mov_b64_e32 v[10:11], v[54:55]
	s_waitcnt vmcnt(3)
	v_mov_b64_e32 v[22:23], v[42:43]
	s_waitcnt vmcnt(2)
	v_mov_b64_e32 v[18:19], v[46:47]
	v_mov_b64_e32 v[4:5], v[64:65]
	s_waitcnt vmcnt(1)
	v_mov_b64_e32 v[26:27], v[38:39]
	s_waitcnt vmcnt(0)
	v_mov_b64_e32 v[30:31], v[34:35]
	v_mov_b64_e32 v[8:9], v[60:61]
	v_mov_b64_e32 v[12:13], v[56:57]
	v_mov_b64_e32 v[16:17], v[52:53]
	v_mov_b64_e32 v[20:21], v[48:49]
	v_mov_b64_e32 v[24:25], v[44:45]
	v_mov_b64_e32 v[28:29], v[40:41]
	v_mov_b64_e32 v[32:33], v[36:37]
	s_branch .LBB0_793

; #define GAS __attribute__((address_space(1)))
; #define LAS __attribute__((address_space(3)))
; #define PHASE_FRAME(F0) Frame F = F0; { int t_ = threadIdx.x; asm volatile("" : "+v"(t_)); F.tid = t_; F.lane = t_ & 63; F.wave = __builtin_amdgcn_readfirstlane(t_ >> 6); }
; __device__ __forceinline__ void titem_load(const TItem& T, int lane, f32x4 (&v)[8]) {
;     const int nblk = T.N / 32, kb = T.item / nblk, nb = T.item % nblk, k0 = 64 * kb, n0 = 32 * nb;
; #pragma unroll
;     for (int i = 0; i < 8; ++i) v[i] = *(const GAS f32x4*)(T.W + (size_t)(k0 + 8 * i + (lane >> 3)) * T.N + n0 + 4 * (lane & 7));
; }
; __device__ __forceinline__ void moe_convert_run(Frame& F, int L, int first, int end, int stride, LAS float* scr) {
;     if (first >= end) return;
;     f32x4 nv[8]; TItem nT = moe_item(F, L, first); titem_load(nT, F.lane, nv);
;     for (int r = first; r < end; r += stride) {
;         const TItem T = nT; f32x4 v[8];
; #pragma unroll
;         for (int i = 0; i < 8; ++i) v[i] = nv[i];
;         if (r + stride < end) { nT = moe_item(F, L, r + stride); titem_load(nT, F.lane, nv); }
;         titem_store(T, F.lane, v, scr);
;     }
; }
; __device__ __forceinline__ void moe_convert_slice(const Frame& F0, int L, int first, int n, int rank, int n_idle) {
;     PHASE_FRAME(F0);
;     const int per = (n + n_idle - 1) / n_idle, lo = first + rank * per, hi = (lo + per < first + n) ? lo + per : first + n;
;     moe_convert_run(F, L, lo + F.wave, hi, 8, (LAS float*)(F.lds + F.wave * 16384));
.LBB0_1099:
	s_mul_hi_i32 s0, s4, 0x2aaaaaab
	s_lshr_b32 s1, s0, 31
	s_ashr_i32 s0, s0, 8
	s_add_i32 s0, s0, s1
	s_lshl_b32 s17, s7, 4
	s_add_i32 s18, s0, s17
	s_lshl_b32 s1, s8, 14
	s_ashr_i32 s19, s18, 31
	s_add_i32 s11, s1, 0
	s_lshl_b64 s[0:1], s[18:19], 20
	s_lshl_b64 s[22:23], s[18:19], 21
	v_readlane_b32 s7, v253, 45
	s_add_u32 s7, s7, s22
	v_readlane_b32 s8, v253, 46
	s_addc_u32 s8, s8, s23
	v_readlane_b32 s22, v253, 43
	s_add_u32 s0, s22, s0
	v_readlane_b32 s22, v253, 44
	s_addc_u32 s1, s22, s1
	s_cmp_lt_i32 s5, 2
	s_cselect_b32 s1, s8, s1
	s_cselect_b32 s0, s7, s0
	s_lshl_b64 s[18:19], s[18:19], 22
	s_add_u32 s8, s9, s18
	s_addc_u32 s9, s10, s19
	s_lshl_b32 s6, s6, 9
	s_sub_i32 s10, s4, s6
	s_bfe_u32 s6, s10, 0x5001a
	s_add_i32 s6, s10, s6
	s_sext_i32_i16 s7, s6
	s_lshl_b32 s7, s7, 1
	v_bfe_u32 v1, v2, 3, 3
	s_andn2_b32 s7, s7, 63
	s_and_b32 s6, s6, 0xffe0
	v_or_b32_e32 v4, s7, v1
	s_sub_i32 s6, s10, s6
	s_sext_i32_i16 s6, s6
	v_or_b32_e32 v20, 8, v4
	s_lshl_b32 s6, s6, 5
	v_or_b32_e32 v10, 48, v4
	v_or_b32_e32 v12, 40, v4
	v_or_b32_e32 v14, 32, v4
	v_or_b32_e32 v16, 24, v4
	v_or_b32_e32 v18, 16, v4
	v_ashrrev_i32_e32 v21, 31, v20
	v_ashrrev_i32_e32 v5, 31, v4
	v_or_b32_e32 v6, 56, v4
	s_ashr_i32 s7, s6, 31
	v_lshlrev_b32_e32 v3, 2, v2
	v_ashrrev_i32_e32 v11, 31, v10
	v_ashrrev_i32_e32 v13, 31, v12
	v_ashrrev_i32_e32 v15, 31, v14
	v_ashrrev_i32_e32 v17, 31, v16
	v_ashrrev_i32_e32 v19, 31, v18
	v_lshlrev_b64 v[20:21], 12, v[20:21]
	v_lshlrev_b64 v[4:5], 12, v[4:5]
	v_ashrrev_i32_e32 v7, 31, v6
	s_lshl_b64 s[6:7], s[6:7], 2
	v_and_b32_e32 v8, 28, v3
	v_lshlrev_b64 v[10:11], 12, v[10:11]
	v_lshlrev_b64 v[12:13], 12, v[12:13]
	v_lshlrev_b64 v[14:15], 12, v[14:15]
	v_lshlrev_b64 v[16:17], 12, v[16:17]
	v_lshlrev_b64 v[18:19], 12, v[18:19]
	v_lshl_add_u64 v[20:21], s[8:9], 0, v[20:21]
	v_lshl_add_u64 v[4:5], s[8:9], 0, v[4:5]
	v_lshlrev_b64 v[6:7], 12, v[6:7]
	v_lshlrev_b32_e32 v190, 2, v8
	v_lshl_add_u64 v[10:11], s[8:9], 0, v[10:11]
	v_lshl_add_u64 v[12:13], s[8:9], 0, v[12:13]
	v_lshl_add_u64 v[14:15], s[8:9], 0, v[14:15]
	v_lshl_add_u64 v[16:17], s[8:9], 0, v[16:17]
	v_lshl_add_u64 v[18:19], s[8:9], 0, v[18:19]
	v_lshl_add_u64 v[20:21], v[20:21], 0, s[6:7]
	v_lshl_add_u64 v[4:5], v[4:5], 0, s[6:7]
	v_lshl_add_u64 v[6:7], s[8:9], 0, v[6:7]
	v_lshl_add_u64 v[10:11], v[10:11], 0, s[6:7]
	v_lshl_add_u64 v[12:13], v[12:13], 0, s[6:7]
	v_lshl_add_u64 v[14:15], v[14:15], 0, s[6:7]
	v_lshl_add_u64 v[16:17], v[16:17], 0, s[6:7]
	v_lshl_add_u64 v[18:19], v[18:19], 0, s[6:7]
	v_lshl_add_u64 v[20:21], v[20:21], 0, v[190:191]
	v_lshl_add_u64 v[4:5], v[4:5], 0, v[190:191]
	v_lshl_add_u64 v[6:7], v[6:7], 0, s[6:7]
	v_lshl_add_u64 v[12:13], v[12:13], 0, v[190:191]
	v_lshl_add_u64 v[14:15], v[14:15], 0, v[190:191]
	v_lshl_add_u64 v[16:17], v[16:17], 0, v[190:191]
	v_lshl_add_u64 v[18:19], v[18:19], 0, v[190:191]
	global_load_dwordx4 v[58:61], v[20:21], off nt
	global_load_dwordx4 v[62:65], v[4:5], off nt
	global_load_dwordx4 v[50:53], v[16:17], off nt
	global_load_dwordx4 v[54:57], v[18:19], off nt
	global_load_dwordx4 v[42:45], v[12:13], off nt
	global_load_dwordx4 v[46:49], v[14:15], off nt
	v_lshl_add_u64 v[4:5], v[10:11], 0, v[190:191]
	v_lshl_add_u64 v[6:7], v[6:7], 0, v[190:191]
	global_load_dwordx4 v[38:41], v[4:5], off nt
	global_load_dwordx4 v[34:37], v[6:7], off nt
	v_lshlrev_b32_e32 v5, 3, v2
	s_cmp_eq_u32 s5, 1
	v_and_b32_e32 v66, 56, v5
	s_cselect_b32 s5, 5, 2
	s_and_b64 s[2:3], s[2:3], exec
	v_add_u32_e32 v3, s11, v190
	v_mul_u32_u24_e32 v4, 0x84, v1
	v_mul_u32_u24_e32 v5, 0x84, v66
	v_bfe_u32 v68, v2, 3, 2
	v_lshlrev_b32_e32 v2, 2, v1
	s_cselect_b32 s23, 4, s5
	v_add3_u32 v69, s11, v5, v2
	v_and_b32_e32 v70, 16, v2
	v_or_b32_e32 v73, 12, v2
	v_lshlrev_b32_e32 v190, 2, v8
	v_add_u32_e32 v74, v3, v4
	v_mov_b32_e32 v67, v191
	v_or_b32_e32 v71, 4, v70
	v_or_b32_e32 v72, 8, v70
	s_add_i32 s22, s4, 8
	s_mov_b32 s28, s10
	s_mov_b32 s25, s23
	s_mov_b64 s[4:5], s[0:1]
	s_waitcnt vmcnt(7)
	v_mov_b64_e32 v[6:7], v[58:59]
	s_waitcnt vmcnt(6)
	v_mov_b64_e32 v[2:3], v[62:63]
	s_waitcnt vmcnt(5)
	v_mov_b64_e32 v[14:15], v[50:51]
	s_waitcnt vmcnt(4)
	v_mov_b64_e32 v[10:11], v[54:55]
	s_waitcnt vmcnt(3)
	v_mov_b64_e32 v[22:23], v[42:43]
	s_waitcnt vmcnt(2)
	v_mov_b64_e32 v[18:19], v[46:47]
	v_mov_b64_e32 v[4:5], v[64:65]
	s_waitcnt vmcnt(1)
	v_mov_b64_e32 v[26:27], v[38:39]
	s_waitcnt vmcnt(0)
	v_mov_b64_e32 v[30:31], v[34:35]
	v_mov_b64_e32 v[8:9], v[60:61]
	v_mov_b64_e32 v[12:13], v[56:57]
	v_mov_b64_e32 v[16:17], v[52:53]
	v_mov_b64_e32 v[20:21], v[48:49]
	v_mov_b64_e32 v[24:25], v[44:45]
	v_mov_b64_e32 v[28:29], v[40:41]
	v_mov_b64_e32 v[32:33], v[36:37]
	s_branch .LBB0_1101

; #define GAS __attribute__((address_space(1)))
; #define LAS __attribute__((address_space(3)))
; #define PHASE_FRAME(F0) Frame F = F0; { int t_ = threadIdx.x; asm volatile("" : "+v"(t_)); F.tid = t_; F.lane = t_ & 63; F.wave = __builtin_amdgcn_readfirstlane(t_ >> 6); }
; __device__ __forceinline__ void titem_load(const TItem& T, int lane, f32x4 (&v)[8]) {
;     const int nblk = T.N / 32, kb = T.item / nblk, nb = T.item % nblk, k0 = 64 * kb, n0 = 32 * nb;
; #pragma unroll
;     for (int i = 0; i < 8; ++i) v[i] = *(const GAS f32x4*)(T.W + (size_t)(k0 + 8 * i + (lane >> 3)) * T.N + n0 + 4 * (lane & 7));
; }
; __device__ __forceinline__ void moe_convert_run(Frame& F, int L, int first, int end, int stride, LAS float* scr) {
;     if (first >= end) return;
;     f32x4 nv[8]; TItem nT = moe_item(F, L, first); titem_load(nT, F.lane, nv);
;     for (int r = first; r < end; r += stride) {
;         const TItem T = nT; f32x4 v[8];
; #pragma unroll
;         for (int i = 0; i < 8; ++i) v[i] = nv[i];
;         if (r + stride < end) { nT = moe_item(F, L, r + stride); titem_load(nT, F.lane, nv); }
;         titem_store(T, F.lane, v, scr);
;     }
; }
; __device__ __forceinline__ void moe_convert_slice(const Frame& F0, int L, int first, int n, int rank, int n_idle) {
;     PHASE_FRAME(F0);
;     const int per = (n + n_idle - 1) / n_idle, lo = first + rank * per, hi = (lo + per < first + n) ? lo + per : first + n;
;     moe_convert_run(F, L, lo + F.wave, hi, 8, (LAS float*)(F.lds + F.wave * 16384));
.LBB0_1516:
	s_mul_hi_i32 s0, s4, 0x2aaaaaab
	s_lshr_b32 s1, s0, 31
	s_ashr_i32 s0, s0, 8
	s_add_i32 s0, s0, s1
	s_lshl_b32 s17, s6, 4
	s_add_i32 s18, s0, s17
	s_lshl_b32 s1, s8, 14
	s_ashr_i32 s19, s18, 31
	s_add_i32 s11, s1, 0
	s_lshl_b64 s[0:1], s[18:19], 20
	s_lshl_b64 s[22:23], s[18:19], 21
	v_readlane_b32 s6, v253, 45
	s_add_u32 s6, s6, s22
	v_readlane_b32 s8, v253, 46
	s_addc_u32 s8, s8, s23
	v_readlane_b32 s22, v253, 43
	s_add_u32 s0, s22, s0
	v_readlane_b32 s22, v253, 44
	s_addc_u32 s1, s22, s1
	s_cmp_lt_i32 s5, 2
	s_cselect_b32 s1, s8, s1
	s_cselect_b32 s0, s6, s0
	s_lshl_b64 s[18:19], s[18:19], 22
	s_add_u32 s8, s9, s18
	s_addc_u32 s9, s10, s19
	s_lshl_b32 s6, s7, 9
	s_sub_i32 s10, s4, s6
	s_bfe_u32 s6, s10, 0x5001a
	s_add_i32 s6, s10, s6
	s_sext_i32_i16 s7, s6
	s_lshl_b32 s7, s7, 1
	v_bfe_u32 v1, v2, 3, 3
	s_andn2_b32 s7, s7, 63
	s_and_b32 s6, s6, 0xffe0
	v_or_b32_e32 v4, s7, v1
	s_sub_i32 s6, s10, s6
	s_sext_i32_i16 s6, s6
	v_or_b32_e32 v20, 8, v4
	s_lshl_b32 s6, s6, 5
	v_or_b32_e32 v10, 48, v4
	v_or_b32_e32 v12, 40, v4
	v_or_b32_e32 v14, 32, v4
	v_or_b32_e32 v16, 24, v4
	v_or_b32_e32 v18, 16, v4
	v_ashrrev_i32_e32 v21, 31, v20
	v_ashrrev_i32_e32 v5, 31, v4
	v_or_b32_e32 v6, 56, v4
	s_ashr_i32 s7, s6, 31
	v_lshlrev_b32_e32 v3, 2, v2
	v_ashrrev_i32_e32 v11, 31, v10
	v_ashrrev_i32_e32 v13, 31, v12
	v_ashrrev_i32_e32 v15, 31, v14
	v_ashrrev_i32_e32 v17, 31, v16
	v_ashrrev_i32_e32 v19, 31, v18
	v_lshlrev_b64 v[20:21], 12, v[20:21]
	v_lshlrev_b64 v[4:5], 12, v[4:5]
	v_ashrrev_i32_e32 v7, 31, v6
	s_lshl_b64 s[6:7], s[6:7], 2
	v_and_b32_e32 v8, 28, v3
	v_lshlrev_b64 v[10:11], 12, v[10:11]
	v_lshlrev_b64 v[12:13], 12, v[12:13]
	v_lshlrev_b64 v[14:15], 12, v[14:15]
	v_lshlrev_b64 v[16:17], 12, v[16:17]
	v_lshlrev_b64 v[18:19], 12, v[18:19]
	v_lshl_add_u64 v[20:21], s[8:9], 0, v[20:21]
	v_lshl_add_u64 v[4:5], s[8:9], 0, v[4:5]
	v_lshlrev_b64 v[6:7], 12, v[6:7]
	v_lshlrev_b32_e32 v190, 2, v8
	v_lshl_add_u64 v[10:11], s[8:9], 0, v[10:11]
	v_lshl_add_u64 v[12:13], s[8:9], 0, v[12:13]
	v_lshl_add_u64 v[14:15], s[8:9], 0, v[14:15]
	v_lshl_add_u64 v[16:17], s[8:9], 0, v[16:17]
	v_lshl_add_u64 v[18:19], s[8:9], 0, v[18:19]
	v_lshl_add_u64 v[20:21], v[20:21], 0, s[6:7]
	v_lshl_add_u64 v[4:5], v[4:5], 0, s[6:7]
	v_lshl_add_u64 v[6:7], s[8:9], 0, v[6:7]
	v_lshl_add_u64 v[10:11], v[10:11], 0, s[6:7]
	v_lshl_add_u64 v[12:13], v[12:13], 0, s[6:7]
	v_lshl_add_u64 v[14:15], v[14:15], 0, s[6:7]
	v_lshl_add_u64 v[16:17], v[16:17], 0, s[6:7]
	v_lshl_add_u64 v[18:19], v[18:19], 0, s[6:7]
	v_lshl_add_u64 v[20:21], v[20:21], 0, v[190:191]
	v_lshl_add_u64 v[4:5], v[4:5], 0, v[190:191]
	v_lshl_add_u64 v[6:7], v[6:7], 0, s[6:7]
	v_lshl_add_u64 v[12:13], v[12:13], 0, v[190:191]
	v_lshl_add_u64 v[14:15], v[14:15], 0, v[190:191]
	v_lshl_add_u64 v[16:17], v[16:17], 0, v[190:191]
	v_lshl_add_u64 v[18:19], v[18:19], 0, v[190:191]
	global_load_dwordx4 v[58:61], v[20:21], off nt
	global_load_dwordx4 v[62:65], v[4:5], off nt
	global_load_dwordx4 v[50:53], v[16:17], off nt
	global_load_dwordx4 v[54:57], v[18:19], off nt
	global_load_dwordx4 v[42:45], v[12:13], off nt
	global_load_dwordx4 v[46:49], v[14:15], off nt
	v_lshl_add_u64 v[4:5], v[10:11], 0, v[190:191]
	v_lshl_add_u64 v[6:7], v[6:7], 0, v[190:191]
	global_load_dwordx4 v[38:41], v[4:5], off nt
	global_load_dwordx4 v[34:37], v[6:7], off nt
	v_lshlrev_b32_e32 v5, 3, v2
	s_cmp_eq_u32 s5, 1
	v_and_b32_e32 v66, 56, v5
	s_cselect_b32 s5, 5, 2
	s_and_b64 s[2:3], s[2:3], exec
	v_add_u32_e32 v3, s11, v190
	v_mul_u32_u24_e32 v4, 0x84, v1
	v_mul_u32_u24_e32 v5, 0x84, v66
	v_bfe_u32 v68, v2, 3, 2
	v_lshlrev_b32_e32 v2, 2, v1
	s_cselect_b32 s23, 4, s5
	v_add3_u32 v69, s11, v5, v2
	v_and_b32_e32 v70, 16, v2
	v_or_b32_e32 v73, 12, v2
	v_lshlrev_b32_e32 v190, 2, v8
	v_add_u32_e32 v74, v3, v4
	v_mov_b32_e32 v67, v191
	v_or_b32_e32 v71, 4, v70
	v_or_b32_e32 v72, 8, v70
	s_add_i32 s22, s4, 8
	s_mov_b32 s28, s10
	s_mov_b32 s25, s23
	s_mov_b64 s[4:5], s[0:1]
	s_waitcnt vmcnt(7)
	v_mov_b64_e32 v[6:7], v[58:59]
	s_waitcnt vmcnt(6)
	v_mov_b64_e32 v[2:3], v[62:63]
	s_waitcnt vmcnt(5)
	v_mov_b64_e32 v[14:15], v[50:51]
	s_waitcnt vmcnt(4)
	v_mov_b64_e32 v[10:11], v[54:55]
	s_waitcnt vmcnt(3)
	v_mov_b64_e32 v[22:23], v[42:43]
	s_waitcnt vmcnt(2)
	v_mov_b64_e32 v[18:19], v[46:47]
	v_mov_b64_e32 v[4:5], v[64:65]
	s_waitcnt vmcnt(1)
	v_mov_b64_e32 v[26:27], v[38:39]
	s_waitcnt vmcnt(0)
	v_mov_b64_e32 v[30:31], v[34:35]
	v_mov_b64_e32 v[8:9], v[60:61]
	v_mov_b64_e32 v[12:13], v[56:57]
	v_mov_b64_e32 v[16:17], v[52:53]
	v_mov_b64_e32 v[20:21], v[48:49]
	v_mov_b64_e32 v[24:25], v[44:45]
	v_mov_b64_e32 v[28:29], v[40:41]
	v_mov_b64_e32 v[32:33], v[36:37]
	s_branch .LBB0_1518
